# v44: v43 without the second-half weight register prefetch, + router logits loop LDS weight reads running four steps ahead of their packed FMAs (five register quads)
# speedup vs baseline: 1.0001x; 1.0001x over previous
; __device__ __forceinline__ void ph9_router(const Frame& F, const Args& A) {
;     ...
;     for (int grp = F.vcu; grp < S_ / 32; grp += F.G) {
;         int lane = F.lane; asm volatile("" : "+v"(lane));
;         const int tid = F.wave * 64 + lane;
;         const int r0 = grp * 32 + F.wave * 4;
;         if (tid < 32) cntL[tid] = 0u;
;         f32x4 hv[4][8];
;         { f32x4 t16[16];
; #pragma unroll
;           for (int i = 0; i < 16; ++i) t16[i] = ((const f32x4*)WRT)[tid + 512 * i];
;           __builtin_amdgcn_sched_barrier(0);
; #pragma unroll
;           for (int r = 0; r < 4; ++r) { const f32x4* xr = (const f32x4*)(X1 + (size_t)(r0 + r) * DM) + lane;
; #pragma unroll
;               for (int j = 0; j < 8; ++j) hv[r][j] = xr[64 * j]; }
;           __builtin_amdgcn_sched_barrier(0);
; #pragma unroll
;           for (int i = 0; i < 16; ++i) wl[tid + 512 * i] = t16[i]; }
.LBB0_1193:
	v_mov_b32_e32 v132, v1
	s_nop 0
	v_add_u32_e32 v134, s44, v132
	v_cmp_gt_i32_e64 s[2:3], 32, v134
	v_lshl_add_u32 v192, v134, 2, 0
	s_and_saveexec_b64 s[0:1], s[2:3]
	v_add_u32_e32 v2, 0x20500, v192
	ds_write_b32 v2, v131
	s_or_b64 exec, exec, s[0:1]
	v_ashrrev_i32_e32 v135, 31, v134
	v_lshl_add_u64 v[2:3], v[134:135], 4, s[20:21]
	v_add_co_u32_e32 v4, vcc, 0x2000, v2
	s_lshl_b32 s0, s52, 5
	s_nop 0
	v_addc_co_u32_e32 v5, vcc, 0, v3, vcc
	global_load_dwordx4 v[136:139], v[2:3], off
	global_load_dwordx4 v[140:143], v[4:5], off
	v_add_co_u32_e32 v4, vcc, 0x4000, v2
	s_add_i32 s40, s0, s45
	s_nop 0
	v_addc_co_u32_e32 v5, vcc, 0, v3, vcc
	v_add_co_u32_e32 v6, vcc, 0x6000, v2
	s_mov_b32 s42, 0
	s_nop 0
	v_addc_co_u32_e32 v7, vcc, 0, v3, vcc
	global_load_dwordx4 v[144:147], v[4:5], off
	global_load_dwordx4 v[148:151], v[6:7], off
	v_add_co_u32_e32 v4, vcc, 0x8000, v2
	s_nop 1
	v_addc_co_u32_e32 v5, vcc, 0, v3, vcc
	v_add_co_u32_e32 v6, vcc, 0xa000, v2
	s_nop 1
	v_addc_co_u32_e32 v7, vcc, 0, v3, vcc
	global_load_dwordx4 v[152:155], v[4:5], off
	global_load_dwordx4 v[156:159], v[6:7], off
	v_add_co_u32_e32 v4, vcc, 0xc000, v2
	s_nop 1
	v_addc_co_u32_e32 v5, vcc, 0, v3, vcc
	v_add_co_u32_e32 v6, vcc, 0xe000, v2
	s_nop 1
	v_addc_co_u32_e32 v7, vcc, 0, v3, vcc
	global_load_dwordx4 v[160:163], v[4:5], off
	global_load_dwordx4 v[164:167], v[6:7], off
	v_add_co_u32_e32 v4, vcc, 0x10000, v2
	s_nop 1
	v_addc_co_u32_e32 v5, vcc, 0, v3, vcc
	v_add_co_u32_e32 v6, vcc, 0x12000, v2
	s_nop 1
	v_addc_co_u32_e32 v7, vcc, 0, v3, vcc
	global_load_dwordx4 v[174:177], v[4:5], off
	global_load_dwordx4 v[194:197], v[6:7], off
	v_add_co_u32_e32 v4, vcc, 0x14000, v2
	s_nop 1
	v_addc_co_u32_e32 v5, vcc, 0, v3, vcc
	v_add_co_u32_e32 v6, vcc, 0x16000, v2
	s_nop 1
	v_addc_co_u32_e32 v7, vcc, 0, v3, vcc
	global_load_dwordx4 v[198:201], v[4:5], off
	global_load_dwordx4 v[202:205], v[6:7], off
	v_add_co_u32_e32 v4, vcc, 0x18000, v2
	s_nop 1
	v_addc_co_u32_e32 v5, vcc, 0, v3, vcc
	v_add_co_u32_e32 v6, vcc, 0x1a000, v2
	s_nop 1
	v_addc_co_u32_e32 v7, vcc, 0, v3, vcc
	global_load_dwordx4 v[206:209], v[4:5], off
	global_load_dwordx4 v[210:213], v[6:7], off
	v_add_co_u32_e32 v4, vcc, 0x1c000, v2
	s_nop 1
	v_addc_co_u32_e32 v5, vcc, 0, v3, vcc
	v_add_co_u32_e32 v2, vcc, 0x1e000, v2
	s_nop 1
	v_addc_co_u32_e32 v3, vcc, 0, v3, vcc
	global_load_dwordx4 v[214:217], v[4:5], off
	global_load_dwordx4 v[218:221], v[2:3], off
	v_readlane_b32 s4, v254, 33
	v_ashrrev_i32_e32 v133, 31, v132
	v_readlane_b32 s5, v254, 34
	s_ashr_i32 s41, s40, 31
	v_readlane_b32 s6, v254, 35
	v_lshl_add_u64 v[2:3], v[132:133], 4, s[4:5]
	s_lshl_b64 s[0:1], s[40:41], 13
	v_readlane_b32 s7, v254, 36
	v_lshl_add_u64 v[4:5], v[2:3], 0, s[0:1]
	s_or_b32 s6, s40, 1
	global_load_dwordx4 v[114:117], v[4:5], off
	global_load_dwordx4 v[102:105], v[4:5], off offset:1024
	global_load_dwordx4 v[94:97], v[4:5], off offset:2048
	global_load_dwordx4 v[90:93], v[4:5], off offset:3072
	v_add_co_u32_e32 v4, vcc, s46, v4
	s_ashr_i32 s7, s6, 31
	s_nop 0
	v_addc_co_u32_e32 v5, vcc, 0, v5, vcc
	s_lshl_b64 s[0:1], s[6:7], 13
	global_load_dwordx4 v[122:125], v[4:5], off
	global_load_dwordx4 v[118:121], v[4:5], off offset:1024
	global_load_dwordx4 v[106:109], v[4:5], off offset:2048
	global_load_dwordx4 v[98:101], v[4:5], off offset:3072
	v_lshl_add_u64 v[4:5], v[2:3], 0, s[0:1]
	s_or_b32 s4, s40, 2
	global_load_dwordx4 v[126:129], v[4:5], off
	global_load_dwordx4 v[110:113], v[4:5], off offset:1024
	global_load_dwordx4 v[86:89], v[4:5], off offset:2048
	global_load_dwordx4 v[82:85], v[4:5], off offset:3072
	v_add_co_u32_e32 v4, vcc, s46, v4
	s_ashr_i32 s5, s4, 31
	s_nop 0
	v_addc_co_u32_e32 v5, vcc, 0, v5, vcc
	s_lshl_b64 s[0:1], s[4:5], 13
	global_load_dwordx4 v[78:81], v[4:5], off
	global_load_dwordx4 v[74:77], v[4:5], off offset:1024
	global_load_dwordx4 v[70:73], v[4:5], off offset:2048
	global_load_dwordx4 v[62:65], v[4:5], off offset:3072
	v_lshl_add_u64 v[4:5], v[2:3], 0, s[0:1]
	s_or_b32 s0, s40, 3
	v_readlane_b32 s8, v254, 37
	v_readlane_b32 s9, v254, 38
	s_ashr_i32 s1, s0, 31
	global_load_dwordx4 v[66:69], v[4:5], off
	global_load_dwordx4 v[58:61], v[4:5], off offset:1024
	global_load_dwordx4 v[54:57], v[4:5], off offset:2048
	global_load_dwordx4 v[50:53], v[4:5], off offset:3072
	v_add_co_u32_e32 v4, vcc, s46, v4
	s_lshl_b64 s[8:9], s[0:1], 13
	s_nop 0
	v_addc_co_u32_e32 v5, vcc, 0, v5, vcc
	v_lshl_add_u64 v[2:3], v[2:3], 0, s[8:9]
	global_load_dwordx4 v[46:49], v[4:5], off
	global_load_dwordx4 v[42:45], v[4:5], off offset:1024
	global_load_dwordx4 v[38:41], v[4:5], off offset:2048
	global_load_dwordx4 v[34:37], v[4:5], off offset:3072
	global_load_dwordx4 v[30:33], v[2:3], off
	global_load_dwordx4 v[26:29], v[2:3], off offset:1024
	global_load_dwordx4 v[22:25], v[2:3], off offset:2048
	global_load_dwordx4 v[18:21], v[2:3], off offset:3072
	v_add_co_u32_e32 v2, vcc, s46, v2
	v_readlane_b32 s10, v254, 39
	s_nop 0
	v_addc_co_u32_e32 v3, vcc, 0, v3, vcc
	global_load_dwordx4 v[14:17], v[2:3], off
	global_load_dwordx4 v[10:13], v[2:3], off offset:1024
	global_load_dwordx4 v[6:9], v[2:3], off offset:2048
	s_nop 0
	global_load_dwordx4 v[2:5], v[2:3], off offset:3072
	v_readlane_b32 s11, v254, 40
	v_readlane_b32 s12, v254, 41
	v_readlane_b32 s13, v254, 42
	v_readlane_b32 s14, v254, 43
	v_readlane_b32 s15, v254, 44
	v_readlane_b32 s16, v254, 45
	v_readlane_b32 s17, v254, 46
	v_readlane_b32 s18, v254, 47
	v_readlane_b32 s19, v254, 48
	v_lshl_add_u32 v135, v134, 4, 0
	v_add_u32_e32 v130, 0x10000, v135
	s_waitcnt vmcnt(47)
	ds_write_b128 v135, v[136:139]
	s_waitcnt vmcnt(46)
	ds_write_b128 v135, v[140:143] offset:8192
	s_waitcnt vmcnt(45)
; __device__ __forceinline__ void ph9_router(const Frame& F, const Args& A) {
;     ...
;           for (int i = 0; i < 16; ++i) wl[tid + 512 * i] = t16[i]; }
;         __builtin_amdgcn_sched_barrier(0);
; #pragma unroll
;         for (int r = 0; r < 4; ++r) { const uint2* dr = (const uint2*)(DX + (size_t)(r0 + r) * DM) + lane; uint2 dw[8];
; #pragma unroll
;             for (int j = 0; j < 8; ++j) dw[j] = dr[64 * j];
; #pragma unroll
;             for (int j = 0; j < 8; ++j) { hv[r][j].x += bflo(dw[j].x); hv[r][j].y += bfhi(dw[j].x); hv[r][j].z += bflo(dw[j].y); hv[r][j].w += bfhi(dw[j].y); } }
	ds_write_b128 v135, v[144:147] offset:16384
	s_waitcnt vmcnt(44)
	ds_write_b128 v135, v[148:151] offset:24576
	s_waitcnt vmcnt(43)
	ds_write_b128 v135, v[152:155] offset:32768
	s_waitcnt vmcnt(42)
	ds_write_b128 v135, v[156:159] offset:40960
	s_waitcnt vmcnt(41)
	ds_write_b128 v135, v[160:163] offset:49152
	s_waitcnt vmcnt(40)
	ds_write_b128 v135, v[164:167] offset:57344
	s_waitcnt vmcnt(39)
	ds_write_b128 v130, v[174:177]
	v_add_u32_e32 v130, 0x12000, v135
	s_waitcnt vmcnt(38)
	ds_write_b128 v130, v[194:197]
	v_add_u32_e32 v130, 0x14000, v135
	s_waitcnt vmcnt(37)
	ds_write_b128 v130, v[198:201]
	v_add_u32_e32 v130, 0x16000, v135
	s_waitcnt vmcnt(36)
	ds_write_b128 v130, v[202:205]
	v_add_u32_e32 v130, 0x18000, v135
	s_waitcnt vmcnt(35)
	ds_write_b128 v130, v[206:209]
	v_add_u32_e32 v130, 0x1a000, v135
	s_waitcnt vmcnt(34)
	ds_write_b128 v130, v[210:213]
	v_add_u32_e32 v130, 0x1c000, v135
	s_waitcnt vmcnt(33)
	ds_write_b128 v130, v[214:217]
	v_add_u32_e32 v130, 0x1e000, v135
	s_waitcnt vmcnt(32)
	ds_write_b128 v130, v[218:221]
	v_lshl_add_u64 v[136:137], v[132:133], 3, s[58:59]
	s_lshl_b64 s[8:9], s[40:41], 12
	v_lshl_add_u64 v[138:139], v[136:137], 0, s[8:9]
	global_load_dwordx2 v[140:141], v[138:139], off
	global_load_dwordx2 v[142:143], v[138:139], off offset:512
	global_load_dwordx2 v[144:145], v[138:139], off offset:1024
	global_load_dwordx2 v[146:147], v[138:139], off offset:1536
	global_load_dwordx2 v[148:149], v[138:139], off offset:2048
	global_load_dwordx2 v[150:151], v[138:139], off offset:2560
	global_load_dwordx2 v[152:153], v[138:139], off offset:3072
	s_nop 0
	global_load_dwordx2 v[138:139], v[138:139], off offset:3584
	s_lshl_b64 s[6:7], s[6:7], 12
	v_lshl_add_u64 v[154:155], v[136:137], 0, s[6:7]
	global_load_dwordx2 v[156:157], v[154:155], off
	global_load_dwordx2 v[164:165], v[154:155], off offset:512
	global_load_dwordx2 v[166:167], v[154:155], off offset:1024
	global_load_dwordx2 v[174:175], v[154:155], off offset:1536
	s_lshl_b64 s[4:5], s[4:5], 12
	v_lshl_add_u64 v[176:177], v[136:137], 0, s[4:5]
	global_load_dwordx2 v[178:179], v[154:155], off offset:2048
	global_load_dwordx2 v[194:195], v[154:155], off offset:2560
	global_load_dwordx2 v[196:197], v[154:155], off offset:3072
	global_load_dwordx2 v[198:199], v[154:155], off offset:3584
	global_load_dwordx2 v[200:201], v[176:177], off
	global_load_dwordx2 v[202:203], v[176:177], off offset:512
	global_load_dwordx2 v[204:205], v[176:177], off offset:1024
	global_load_dwordx2 v[206:207], v[176:177], off offset:1536
	global_load_dwordx2 v[208:209], v[176:177], off offset:2048
	s_lshl_b64 s[0:1], s[0:1], 12
	v_cmp_lt_i32_e32 vcc, v182, v181
	s_waitcnt vmcnt(20)
	v_lshlrev_b32_e32 v154, 16, v140
	s_waitcnt vmcnt(19)
	v_lshlrev_b32_e32 v160, 16, v142
	v_and_b32_e32 v161, 0xffff0000, v142
	v_lshlrev_b32_e32 v142, 16, v143
	v_and_b32_e32 v143, 0xffff0000, v143
	s_waitcnt vmcnt(17)
	v_lshlrev_b32_e32 v210, 16, v146
	v_and_b32_e32 v211, 0xffff0000, v146
	s_waitcnt vmcnt(15)
	v_lshlrev_b32_e32 v218, 16, v150
	v_and_b32_e32 v219, 0xffff0000, v150
	v_lshlrev_b32_e32 v214, 16, v148
	v_and_b32_e32 v215, 0xffff0000, v148
	v_lshlrev_b32_e32 v216, 16, v149
	v_and_b32_e32 v217, 0xffff0000, v149
	v_pk_add_f32 v[148:149], v[104:105], v[142:143]
	v_pk_add_f32 v[104:105], v[90:91], v[210:211]
	v_pk_add_f32 v[90:91], v[118:119], v[218:219]
	global_load_dwordx2 v[118:119], v[176:177], off offset:2560
	v_and_b32_e32 v155, 0xffff0000, v140
	v_lshlrev_b32_e32 v140, 16, v141
	v_and_b32_e32 v141, 0xffff0000, v141
	v_lshlrev_b32_e32 v212, 16, v147
	v_and_b32_e32 v213, 0xffff0000, v147
	v_lshlrev_b32_e32 v150, 16, v151
	v_and_b32_e32 v151, 0xffff0000, v151
	v_pk_add_f32 v[158:159], v[116:117], v[140:141]
	v_pk_add_f32 v[116:117], v[92:93], v[212:213]
	v_pk_add_f32 v[92:93], v[120:121], v[150:151]
	global_load_dwordx2 v[120:121], v[176:177], off offset:3072
	s_waitcnt vmcnt(15)
	v_lshlrev_b32_e32 v222, 16, v138
	v_and_b32_e32 v223, 0xffff0000, v138
	s_waitcnt vmcnt(14)
	v_lshlrev_b32_e32 v224, 16, v156
	v_and_b32_e32 v225, 0xffff0000, v156
	v_lshlrev_b32_e32 v226, 16, v157
	v_and_b32_e32 v227, 0xffff0000, v157
	v_pk_add_f32 v[156:157], v[114:115], v[154:155]
	v_pk_add_f32 v[114:115], v[98:99], v[222:223]
	s_waitcnt vmcnt(13)
	v_lshlrev_b32_e32 v98, 16, v165
	v_and_b32_e32 v99, 0xffff0000, v165
	v_lshlrev_b32_e32 v162, 16, v144
	v_and_b32_e32 v163, 0xffff0000, v144
	v_lshlrev_b32_e32 v144, 16, v145
	v_and_b32_e32 v145, 0xffff0000, v145
	v_lshlrev_b32_e32 v138, 16, v139
	v_and_b32_e32 v139, 0xffff0000, v139
	v_pk_add_f32 v[154:155], v[112:113], v[98:99]
	s_waitcnt vmcnt(12)
	v_lshlrev_b32_e32 v98, 16, v166
	v_and_b32_e32 v99, 0xffff0000, v166
	v_lshlrev_b32_e32 v220, 16, v152
	v_and_b32_e32 v221, 0xffff0000, v152
	v_lshlrev_b32_e32 v152, 16, v153
	v_and_b32_e32 v153, 0xffff0000, v153
	v_pk_add_f32 v[140:141], v[94:95], v[162:163]
	v_pk_add_f32 v[142:143], v[96:97], v[144:145]
	v_pk_add_f32 v[96:97], v[122:123], v[214:215]
	v_pk_add_f32 v[122:123], v[100:101], v[138:139]
	v_pk_add_f32 v[162:163], v[128:129], v[226:227]
	v_pk_add_f32 v[128:129], v[86:87], v[98:99]
	v_lshlrev_b32_e32 v86, 16, v167
	v_and_b32_e32 v87, 0xffff0000, v167
	global_load_dwordx2 v[138:139], v[176:177], off offset:3584
	v_pk_add_f32 v[94:95], v[106:107], v[220:221]
	v_pk_add_f32 v[106:107], v[108:109], v[152:153]
	v_pk_add_f32 v[144:145], v[88:89], v[86:87]
	s_waitcnt vmcnt(12)
	v_lshlrev_b32_e32 v86, 16, v174
	v_and_b32_e32 v87, 0xffff0000, v174
	v_lshl_add_u64 v[152:153], v[136:137], 0, s[0:1]
	v_lshlrev_b32_e32 v228, 16, v164
	v_and_b32_e32 v229, 0xffff0000, v164
	v_pk_add_f32 v[86:87], v[82:83], v[86:87]
	v_lshlrev_b32_e32 v82, 16, v175
	v_and_b32_e32 v83, 0xffff0000, v175
	global_load_dwordx2 v[164:165], v[152:153], off
	global_load_dwordx2 v[166:167], v[152:153], off offset:512
	v_pk_add_f32 v[88:89], v[84:85], v[82:83]
	s_waitcnt vmcnt(13)
; __device__ __forceinline__ void ph9_router(const Frame& F, const Args& A) {
;     ...
;         for (int r = 0; r < 4; ++r) { const uint2* dr = (const uint2*)(DX + (size_t)(r0 + r) * DM) + lane; uint2 dw[8];
; #pragma unroll
;             for (int j = 0; j < 8; ++j) dw[j] = dr[64 * j];
; #pragma unroll
;             for (int j = 0; j < 8; ++j) { hv[r][j].x += bflo(dw[j].x); hv[r][j].y += bfhi(dw[j].x); hv[r][j].z += bflo(dw[j].y); hv[r][j].w += bfhi(dw[j].y); } }
	v_lshlrev_b32_e32 v82, 16, v178
	v_and_b32_e32 v83, 0xffff0000, v178
	v_pk_add_f32 v[78:79], v[78:79], v[82:83]
	v_lshlrev_b32_e32 v82, 16, v179
	v_and_b32_e32 v83, 0xffff0000, v179
	v_pk_add_f32 v[100:101], v[80:81], v[82:83]
	s_waitcnt vmcnt(12)
	v_lshlrev_b32_e32 v80, 16, v194
	v_and_b32_e32 v81, 0xffff0000, v194
	v_pk_add_f32 v[82:83], v[74:75], v[80:81]
	v_lshlrev_b32_e32 v74, 16, v195
	global_load_dwordx2 v[80:81], v[152:153], off offset:1024
	v_and_b32_e32 v75, 0xffff0000, v195
	v_pk_add_f32 v[84:85], v[76:77], v[74:75]
	s_waitcnt vmcnt(12)
	v_lshlrev_b32_e32 v74, 16, v196
	v_and_b32_e32 v75, 0xffff0000, v196
	v_pk_add_f32 v[98:99], v[70:71], v[74:75]
	global_load_dwordx2 v[74:75], v[152:153], off offset:1536
	global_load_dwordx2 v[76:77], v[152:153], off offset:2048
	global_load_dwordx2 v[174:175], v[152:153], off offset:2560
	v_lshlrev_b32_e32 v70, 16, v197
	v_and_b32_e32 v71, 0xffff0000, v197
	v_pk_add_f32 v[108:109], v[72:73], v[70:71]
	s_waitcnt vmcnt(14)
	v_lshlrev_b32_e32 v70, 16, v198
	v_and_b32_e32 v71, 0xffff0000, v198
	v_pk_add_f32 v[150:151], v[110:111], v[228:229]
	v_pk_add_f32 v[110:111], v[62:63], v[70:71]
	v_lshlrev_b32_e32 v62, 16, v199
	v_and_b32_e32 v63, 0xffff0000, v199
	v_pk_add_f32 v[146:147], v[102:103], v[160:161]
	v_pk_add_f32 v[102:103], v[124:125], v[216:217]
	v_pk_add_f32 v[124:125], v[64:65], v[62:63]
	s_waitcnt vmcnt(13)
	v_lshlrev_b32_e32 v62, 16, v200
	v_and_b32_e32 v63, 0xffff0000, v200
	v_pk_add_f32 v[72:73], v[66:67], v[62:63]
	v_lshlrev_b32_e32 v62, 16, v201
	v_and_b32_e32 v63, 0xffff0000, v201
	v_pk_add_f32 v[68:69], v[68:69], v[62:63]
	s_waitcnt vmcnt(12)
	v_lshlrev_b32_e32 v62, 16, v202
	v_and_b32_e32 v63, 0xffff0000, v202
	v_pk_add_f32 v[62:63], v[58:59], v[62:63]
	v_lshlrev_b32_e32 v58, 16, v203
	v_and_b32_e32 v59, 0xffff0000, v203
	v_pk_add_f32 v[64:65], v[60:61], v[58:59]
	s_waitcnt vmcnt(11)
	v_lshlrev_b32_e32 v58, 16, v204
	v_and_b32_e32 v59, 0xffff0000, v204
	v_pk_add_f32 v[54:55], v[54:55], v[58:59]
	v_lshlrev_b32_e32 v58, 16, v205
	v_and_b32_e32 v59, 0xffff0000, v205
	v_pk_add_f32 v[56:57], v[56:57], v[58:59]
	s_waitcnt vmcnt(10)
	v_lshlrev_b32_e32 v58, 16, v206
	v_and_b32_e32 v59, 0xffff0000, v206
	v_pk_add_f32 v[50:51], v[50:51], v[58:59]
	v_lshlrev_b32_e32 v58, 16, v207
	v_and_b32_e32 v59, 0xffff0000, v207
	v_pk_add_f32 v[58:59], v[52:53], v[58:59]
	s_waitcnt vmcnt(9)
	v_lshlrev_b32_e32 v52, 16, v208
	v_and_b32_e32 v53, 0xffff0000, v208
	v_pk_add_f32 v[66:67], v[46:47], v[52:53]
	v_lshlrev_b32_e32 v46, 16, v209
	v_and_b32_e32 v47, 0xffff0000, v209
	v_pk_add_f32 v[70:71], v[48:49], v[46:47]
	s_waitcnt vmcnt(8)
	v_lshlrev_b32_e32 v46, 16, v118
	v_and_b32_e32 v47, 0xffff0000, v118
	v_pk_add_f32 v[112:113], v[42:43], v[46:47]
	v_lshlrev_b32_e32 v42, 16, v119
	v_and_b32_e32 v43, 0xffff0000, v119
	v_pk_add_f32 v[160:161], v[126:127], v[224:225]
	v_pk_add_f32 v[126:127], v[44:45], v[42:43]
	s_waitcnt vmcnt(7)
	v_lshlrev_b32_e32 v42, 16, v120
	v_and_b32_e32 v43, 0xffff0000, v120
	v_pk_add_f32 v[118:119], v[38:39], v[42:43]
	global_load_dwordx2 v[44:45], v[152:153], off offset:3072
	global_load_dwordx2 v[42:43], v[152:153], off offset:3584
	v_lshlrev_b32_e32 v38, 16, v121
	v_and_b32_e32 v39, 0xffff0000, v121
	v_pk_add_f32 v[120:121], v[40:41], v[38:39]
	s_waitcnt vmcnt(8)
	v_lshlrev_b32_e32 v38, 16, v138
	v_and_b32_e32 v39, 0xffff0000, v138
	v_pk_add_f32 v[136:137], v[34:35], v[38:39]
	v_lshlrev_b32_e32 v34, 16, v139
	v_and_b32_e32 v35, 0xffff0000, v139
	v_pk_add_f32 v[138:139], v[36:37], v[34:35]
	s_waitcnt vmcnt(7)
	v_lshlrev_b32_e32 v34, 16, v164
	v_and_b32_e32 v35, 0xffff0000, v164
	v_pk_add_f32 v[38:39], v[30:31], v[34:35]
	v_lshlrev_b32_e32 v30, 16, v165
	v_and_b32_e32 v31, 0xffff0000, v165
	v_pk_add_f32 v[40:41], v[32:33], v[30:31]
	s_waitcnt vmcnt(6)
	v_lshlrev_b32_e32 v30, 16, v166
	v_and_b32_e32 v31, 0xffff0000, v166
	v_pk_add_f32 v[32:33], v[26:27], v[30:31]
	v_lshlrev_b32_e32 v26, 16, v167
	v_and_b32_e32 v27, 0xffff0000, v167
	v_pk_add_f32 v[28:29], v[28:29], v[26:27]
	s_waitcnt vmcnt(5)
	v_lshlrev_b32_e32 v26, 16, v80
	v_and_b32_e32 v27, 0xffff0000, v80
	v_pk_add_f32 v[34:35], v[22:23], v[26:27]
	v_lshlrev_b32_e32 v22, 16, v81
	v_and_b32_e32 v23, 0xffff0000, v81
	v_pk_add_f32 v[36:37], v[24:25], v[22:23]
	s_waitcnt vmcnt(4)
	v_lshlrev_b32_e32 v22, 16, v74
	v_and_b32_e32 v23, 0xffff0000, v74
	v_pk_add_f32 v[46:47], v[18:19], v[22:23]
	v_lshlrev_b32_e32 v18, 16, v75
	v_and_b32_e32 v19, 0xffff0000, v75
	v_pk_add_f32 v[60:61], v[20:21], v[18:19]
	s_waitcnt vmcnt(3)
	v_lshlrev_b32_e32 v18, 16, v76
	v_and_b32_e32 v19, 0xffff0000, v76
	v_pk_add_f32 v[74:75], v[14:15], v[18:19]
	v_lshlrev_b32_e32 v14, 16, v77
	v_and_b32_e32 v15, 0xffff0000, v77
	v_pk_add_f32 v[164:165], v[16:17], v[14:15]
	s_waitcnt vmcnt(2)
; __device__ __forceinline__ void ph9_router(const Frame& F, const Args& A) {
;     ...
;         for (int r = 0; r < 4; ++r) { const uint2* dr = (const uint2*)(DX + (size_t)(r0 + r) * DM) + lane; uint2 dw[8];
; #pragma unroll
;             for (int j = 0; j < 8; ++j) dw[j] = dr[64 * j];
; #pragma unroll
;             for (int j = 0; j < 8; ++j) { hv[r][j].x += bflo(dw[j].x); hv[r][j].y += bfhi(dw[j].x); hv[r][j].z += bflo(dw[j].y); hv[r][j].w += bfhi(dw[j].y); } }
;         float rstd[4];
; #pragma unroll
;         for (int r = 0; r < 4; ++r) { float ss = 0.f;
; #pragma unroll
;             for (int j = 0; j < 8; ++j) ss += (hv[r][j].x * hv[r][j].x + hv[r][j].y * hv[r][j].y) + (hv[r][j].z * hv[r][j].z + hv[r][j].w * hv[r][j].w);
;             rstd[r] = 1.f / sqrtf(wave_sum(ss) * (1.f / DM) + EPS_); }
	v_lshlrev_b32_e32 v14, 16, v174
	v_and_b32_e32 v15, 0xffff0000, v174
	v_pk_add_f32 v[152:153], v[10:11], v[14:15]
	v_cndmask_b32_e32 v14, v180, v182, vcc
	v_mov_b32_e32 v16, v157
	v_mov_b32_e32 v17, v147
	v_lshlrev_b32_e32 v193, 2, v14
	v_mov_b32_e32 v14, v156
	v_mov_b32_e32 v15, v146
	v_pk_mul_f32 v[16:17], v[16:17], v[16:17]
	v_mov_b32_e32 v18, v159
	v_mov_b32_e32 v19, v149
	v_pk_fma_f32 v[14:15], v[14:15], v[14:15], v[16:17]
	v_mov_b32_e32 v16, v158
	v_mov_b32_e32 v17, v148
	v_pk_mul_f32 v[18:19], v[18:19], v[18:19]
	v_mul_f32_e32 v20, v117, v117
	v_pk_fma_f32 v[16:17], v[16:17], v[16:17], v[18:19]
	v_mov_b32_e32 v18, v141
	v_mov_b32_e32 v19, v143
	v_pk_add_f32 v[14:15], v[14:15], v[16:17]
	v_mov_b32_e32 v16, v140
	v_mov_b32_e32 v17, v142
	v_pk_mul_f32 v[18:19], v[18:19], v[18:19]
	v_pk_add_f32 v[14:15], v[14:15], v[14:15] op_sel:[0,1] op_sel_hi:[1,0]
	v_pk_fma_f32 v[16:17], v[16:17], v[16:17], v[18:19]
	v_mul_f32_e32 v18, v105, v105
	v_pk_add_f32 v[16:17], v[16:17], v[16:17] op_sel:[0,1] op_sel_hi:[1,0]
	v_pk_fma_f32 v[18:19], v[104:105], v[104:105], v[18:19] op_sel_hi:[1,1,0]
	v_pk_fma_f32 v[20:21], v[116:117], v[116:117], v[20:21] op_sel_hi:[1,1,0]
	v_pk_mul_f32 v[22:23], v[96:97], v[96:97]
	v_pk_mul_f32 v[24:25], v[102:103], v[102:103]
	v_mov_b32_e32 v15, v22
	v_mov_b32_e32 v17, v23
	v_mov_b32_e32 v19, v24
	v_mov_b32_e32 v21, v25
	v_pk_add_f32 v[14:15], v[14:15], v[16:17]
	v_pk_add_f32 v[16:17], v[18:19], v[20:21]
	v_mov_b32_e32 v18, v91
	v_mov_b32_e32 v19, v93
	v_pk_add_f32 v[14:15], v[14:15], v[16:17]
	v_mov_b32_e32 v16, v90
	v_mov_b32_e32 v17, v92
	v_pk_mul_f32 v[18:19], v[18:19], v[18:19]
	v_mul_f32_e32 v20, v107, v107
	v_pk_fma_f32 v[16:17], v[16:17], v[16:17], v[18:19]
	v_mul_f32_e32 v18, v95, v95
	v_pk_add_f32 v[14:15], v[14:15], v[14:15] op_sel:[0,1] op_sel_hi:[1,0]
	v_pk_add_f32 v[16:17], v[16:17], v[16:17] op_sel:[0,1] op_sel_hi:[1,0]
	v_pk_fma_f32 v[18:19], v[94:95], v[94:95], v[18:19] op_sel_hi:[1,1,0]
	v_pk_fma_f32 v[20:21], v[106:107], v[106:107], v[20:21] op_sel_hi:[1,1,0]
	v_pk_mul_f32 v[22:23], v[114:115], v[114:115]
	v_pk_mul_f32 v[24:25], v[122:123], v[122:123]
	v_mov_b32_e32 v15, v22
	v_mov_b32_e32 v17, v23
	v_mov_b32_e32 v19, v24
	v_mov_b32_e32 v21, v25
	v_pk_add_f32 v[14:15], v[14:15], v[16:17]
	v_pk_add_f32 v[16:17], v[18:19], v[20:21]
	v_lshlrev_b32_e32 v10, 16, v175
	v_pk_add_f32 v[14:15], v[14:15], v[16:17]
	v_and_b32_e32 v11, 0xffff0000, v175
	v_add_f32_e32 v14, v14, v15
	ds_bpermute_b32 v15, v193, v14
	v_cmp_lt_i32_e32 vcc, v183, v181
	v_pk_add_f32 v[166:167], v[12:13], v[10:11]
	v_mov_b32_e32 v16, v163
	v_cndmask_b32_e32 v10, v180, v183, vcc
	v_lshlrev_b32_e32 v196, 2, v10
	s_waitcnt lgkmcnt(0)
	v_add_f32_e32 v11, v14, v15
	ds_bpermute_b32 v12, v196, v11
	v_cmp_lt_i32_e32 vcc, v184, v181
	s_waitcnt vmcnt(1)
	v_lshlrev_b32_e32 v10, 16, v44
	v_mov_b32_e32 v15, v151
	v_cndmask_b32_e32 v13, v180, v184, vcc
	v_lshlrev_b32_e32 v195, 2, v13
	s_waitcnt lgkmcnt(0)
	v_add_f32_e32 v12, v11, v12
	ds_bpermute_b32 v13, v195, v12
	v_cmp_lt_i32_e32 vcc, v185, v181
	v_and_b32_e32 v11, 0xffff0000, v44
	v_pk_add_f32 v[6:7], v[6:7], v[10:11]
	v_cndmask_b32_e32 v14, v180, v185, vcc
	v_lshlrev_b32_e32 v194, 2, v14
	s_waitcnt lgkmcnt(0)
	v_add_f32_e32 v12, v12, v13
	ds_bpermute_b32 v13, v194, v12
	v_cmp_lt_i32_e32 vcc, v186, v181
	v_mov_b32_e32 v14, v161
	v_pk_mul_f32 v[14:15], v[14:15], v[14:15]
	v_cndmask_b32_e32 v10, v180, v186, vcc
	v_lshlrev_b32_e32 v197, 2, v10
	s_waitcnt lgkmcnt(0)
	v_add_f32_e32 v11, v12, v13
	ds_bpermute_b32 v12, v197, v11
	v_cmp_lt_i32_e32 vcc, v187, v181
	v_mov_b32_e32 v17, v155
	v_pk_mul_f32 v[16:17], v[16:17], v[16:17]
	v_cndmask_b32_e32 v13, v180, v187, vcc
	v_lshlrev_b32_e32 v198, 2, v13
	s_waitcnt lgkmcnt(0)
	v_add_f32_e32 v12, v11, v12
	ds_bpermute_b32 v13, v198, v12
	v_mul_f32_e32 v18, v89, v89
	v_pk_fma_f32 v[18:19], v[88:89], v[88:89], v[18:19] op_sel_hi:[1,1,0]
	v_pk_mul_f32 v[20:21], v[78:79], v[78:79]
	v_pk_mul_f32 v[22:23], v[100:101], v[100:101]
	s_waitcnt lgkmcnt(0)
	v_add_f32_e32 v12, v12, v13
	v_fmamk_f32 v12, v12, 0x3a000000, v169
	v_mul_f32_e32 v13, 0x4f800000, v12
	v_cmp_gt_f32_e32 vcc, s47, v12
	v_mov_b32_e32 v19, v23
	v_lshlrev_b32_e32 v10, 16, v45
	v_cndmask_b32_e32 v24, v12, v13, vcc
	v_mov_b32_e32 v12, v160
	v_mov_b32_e32 v13, v150
	v_pk_fma_f32 v[12:13], v[12:13], v[12:13], v[14:15]
	v_mov_b32_e32 v14, v162
	v_mov_b32_e32 v15, v154
	v_pk_fma_f32 v[14:15], v[14:15], v[14:15], v[16:17]
	v_mov_b32_e32 v16, v129
	v_mov_b32_e32 v17, v145
	v_pk_add_f32 v[12:13], v[12:13], v[14:15]
	v_mov_b32_e32 v14, v128
	v_mov_b32_e32 v15, v144
	v_pk_mul_f32 v[16:17], v[16:17], v[16:17]
	v_pk_add_f32 v[12:13], v[12:13], v[12:13] op_sel:[0,1] op_sel_hi:[1,0]
	v_pk_fma_f32 v[14:15], v[14:15], v[14:15], v[16:17]
	v_mul_f32_e32 v16, v87, v87
	v_pk_add_f32 v[14:15], v[14:15], v[14:15] op_sel:[0,1] op_sel_hi:[1,0]
	v_pk_fma_f32 v[16:17], v[86:87], v[86:87], v[16:17] op_sel_hi:[1,1,0]
	v_mov_b32_e32 v13, v20
	v_mov_b32_e32 v15, v21
	v_mov_b32_e32 v17, v22
	v_pk_add_f32 v[12:13], v[12:13], v[14:15]
	v_pk_add_f32 v[14:15], v[16:17], v[18:19]
	v_mov_b32_e32 v16, v83
	v_mov_b32_e32 v17, v85
	v_pk_add_f32 v[12:13], v[12:13], v[14:15]
	v_mov_b32_e32 v14, v82
	v_mov_b32_e32 v15, v84
	v_pk_mul_f32 v[16:17], v[16:17], v[16:17]
	v_mul_f32_e32 v18, v109, v109
	v_pk_fma_f32 v[14:15], v[14:15], v[14:15], v[16:17]
	v_mul_f32_e32 v16, v99, v99
	v_pk_add_f32 v[12:13], v[12:13], v[12:13] op_sel:[0,1] op_sel_hi:[1,0]
	v_pk_add_f32 v[14:15], v[14:15], v[14:15] op_sel:[0,1] op_sel_hi:[1,0]
	v_pk_fma_f32 v[16:17], v[98:99], v[98:99], v[16:17] op_sel_hi:[1,1,0]
	v_pk_fma_f32 v[18:19], v[108:109], v[108:109], v[18:19] op_sel_hi:[1,1,0]
	v_pk_mul_f32 v[20:21], v[110:111], v[110:111]
	v_pk_mul_f32 v[22:23], v[124:125], v[124:125]
	v_mov_b32_e32 v13, v20
	v_mov_b32_e32 v15, v21
	v_mov_b32_e32 v17, v22
	v_mov_b32_e32 v19, v23
	v_pk_add_f32 v[12:13], v[12:13], v[14:15]
	v_pk_add_f32 v[14:15], v[16:17], v[18:19]
	v_sqrt_f32_e32 v25, v24
	v_pk_add_f32 v[12:13], v[12:13], v[14:15]
	v_and_b32_e32 v11, 0xffff0000, v45
	v_add_f32_e32 v12, v12, v13
	ds_bpermute_b32 v13, v193, v12
	v_pk_add_f32 v[8:9], v[8:9], v[10:11]
	s_waitcnt vmcnt(0)
; __device__ __forceinline__ void ph9_router(const Frame& F, const Args& A) {
;     ...
;         float rstd[4];
; #pragma unroll
;         for (int r = 0; r < 4; ++r) { float ss = 0.f;
; #pragma unroll
;             for (int j = 0; j < 8; ++j) ss += (hv[r][j].x * hv[r][j].x + hv[r][j].y * hv[r][j].y) + (hv[r][j].z * hv[r][j].z + hv[r][j].w * hv[r][j].w);
;             rstd[r] = 1.f / sqrtf(wave_sum(ss) * (1.f / DM) + EPS_); }
	v_lshlrev_b32_e32 v10, 16, v42
	v_and_b32_e32 v11, 0xffff0000, v42
	v_pk_add_f32 v[2:3], v[2:3], v[10:11]
	s_waitcnt lgkmcnt(0)
	v_add_f32_e32 v12, v12, v13
	ds_bpermute_b32 v13, v196, v12
	v_add_u32_e32 v11, -1, v25
	v_fma_f32 v14, -v11, v25, v24
	v_cmp_ge_f32_e64 s[0:1], 0, v14
	v_add_u32_e32 v14, 1, v25
	s_waitcnt lgkmcnt(0)
	v_add_f32_e32 v12, v12, v13
	ds_bpermute_b32 v13, v195, v12
	v_fma_f32 v15, -v14, v25, v24
	v_cndmask_b32_e64 v11, v25, v11, s[0:1]
	v_cmp_lt_f32_e64 s[0:1], 0, v15
	v_lshlrev_b32_e32 v10, 16, v43
	s_waitcnt lgkmcnt(0)
	v_add_f32_e32 v12, v12, v13
	ds_bpermute_b32 v13, v194, v12
	v_cndmask_b32_e64 v11, v11, v14, s[0:1]
	v_mul_f32_e32 v14, 0x37800000, v11
	v_cndmask_b32_e32 v11, v11, v14, vcc
	v_cmp_class_f32_e32 vcc, v24, v171
	s_waitcnt lgkmcnt(0)
	v_add_f32_e32 v12, v12, v13
	ds_bpermute_b32 v13, v197, v12
	v_cndmask_b32_e32 v22, v11, v24, vcc
	v_div_scale_f32 v23, s[0:1], v22, v22, 1.0
	v_rcp_f32_e32 v24, v23
	v_and_b32_e32 v11, 0xffff0000, v43
	v_pk_add_f32 v[4:5], v[4:5], v[10:11]
	v_mov_b32_e32 v14, v69
	v_fma_f32 v10, -v23, v24, 1.0
	v_fmac_f32_e32 v24, v10, v24
	s_waitcnt lgkmcnt(0)
	v_add_f32_e32 v10, v12, v13
	ds_bpermute_b32 v11, v198, v10
	v_mov_b32_e32 v12, v73
	v_mov_b32_e32 v13, v63
	v_pk_mul_f32 v[12:13], v[12:13], v[12:13]
	v_mov_b32_e32 v15, v65
	s_waitcnt lgkmcnt(0)
	v_add_f32_e32 v10, v10, v11
	v_fmamk_f32 v10, v10, 0x3a000000, v169
	v_mul_f32_e32 v11, 0x4f800000, v10
	v_cmp_gt_f32_e64 s[0:1], s47, v10
	v_pk_mul_f32 v[14:15], v[14:15], v[14:15]
	v_mul_f32_e32 v16, v59, v59
	v_cndmask_b32_e64 v30, v10, v11, s[0:1]
	v_mov_b32_e32 v10, v72
	v_mov_b32_e32 v11, v62
	v_pk_fma_f32 v[10:11], v[10:11], v[10:11], v[12:13]
	v_mov_b32_e32 v12, v68
	v_mov_b32_e32 v13, v64
	v_pk_fma_f32 v[12:13], v[12:13], v[12:13], v[14:15]
	v_mov_b32_e32 v14, v55
	v_mov_b32_e32 v15, v57
	v_pk_add_f32 v[10:11], v[10:11], v[12:13]
	v_mov_b32_e32 v12, v54
	v_mov_b32_e32 v13, v56
	v_pk_mul_f32 v[14:15], v[14:15], v[14:15]
	v_pk_add_f32 v[10:11], v[10:11], v[10:11] op_sel:[0,1] op_sel_hi:[1,0]
	v_pk_fma_f32 v[12:13], v[12:13], v[12:13], v[14:15]
	v_mul_f32_e32 v14, v51, v51
	v_pk_add_f32 v[12:13], v[12:13], v[12:13] op_sel:[0,1] op_sel_hi:[1,0]
	v_pk_fma_f32 v[14:15], v[50:51], v[50:51], v[14:15] op_sel_hi:[1,1,0]
	v_pk_fma_f32 v[16:17], v[58:59], v[58:59], v[16:17] op_sel_hi:[1,1,0]
	v_pk_mul_f32 v[18:19], v[66:67], v[66:67]
	v_pk_mul_f32 v[20:21], v[70:71], v[70:71]
	v_mov_b32_e32 v11, v18
	v_mov_b32_e32 v13, v19
	v_mov_b32_e32 v15, v20
	v_mov_b32_e32 v17, v21
	v_pk_add_f32 v[10:11], v[10:11], v[12:13]
	v_pk_add_f32 v[12:13], v[14:15], v[16:17]
	v_mov_b32_e32 v14, v113
	v_mov_b32_e32 v15, v127
	v_pk_add_f32 v[10:11], v[10:11], v[12:13]
	v_mov_b32_e32 v12, v112
	v_mov_b32_e32 v13, v126
	v_pk_mul_f32 v[14:15], v[14:15], v[14:15]
	v_mul_f32_e32 v16, v121, v121
	v_pk_fma_f32 v[12:13], v[12:13], v[12:13], v[14:15]
	v_mul_f32_e32 v14, v119, v119
	v_pk_add_f32 v[10:11], v[10:11], v[10:11] op_sel:[0,1] op_sel_hi:[1,0]
	v_pk_add_f32 v[12:13], v[12:13], v[12:13] op_sel:[0,1] op_sel_hi:[1,0]
	v_pk_fma_f32 v[14:15], v[118:119], v[118:119], v[14:15] op_sel_hi:[1,1,0]
	v_pk_fma_f32 v[16:17], v[120:121], v[120:121], v[16:17] op_sel_hi:[1,1,0]
	v_pk_mul_f32 v[18:19], v[136:137], v[136:137]
	v_pk_mul_f32 v[20:21], v[138:139], v[138:139]
	v_mov_b32_e32 v11, v18
	v_mov_b32_e32 v13, v19
	v_mov_b32_e32 v15, v20
	v_mov_b32_e32 v17, v21
	v_pk_add_f32 v[10:11], v[10:11], v[12:13]
	v_pk_add_f32 v[12:13], v[14:15], v[16:17]
	v_sqrt_f32_e32 v31, v30
	v_pk_add_f32 v[10:11], v[10:11], v[12:13]
	v_div_scale_f32 v25, vcc, 1.0, v22, 1.0
	v_add_f32_e32 v10, v10, v11
	ds_bpermute_b32 v11, v193, v10
	v_add_u32_e32 v13, -1, v31
	v_fma_f32 v14, -v13, v31, v30
	v_cmp_ge_f32_e64 s[4:5], 0, v14
	v_add_u32_e32 v14, 1, v31
	s_waitcnt lgkmcnt(0)
	v_add_f32_e32 v10, v10, v11
	ds_bpermute_b32 v11, v196, v10
	v_fma_f32 v15, -v14, v31, v30
	v_cndmask_b32_e64 v13, v31, v13, s[4:5]
	v_cmp_lt_f32_e64 s[4:5], 0, v15
	v_mul_f32_e32 v26, v25, v24
	s_waitcnt lgkmcnt(0)
	v_add_f32_e32 v10, v10, v11
	ds_bpermute_b32 v11, v195, v10
	v_cndmask_b32_e64 v13, v13, v14, s[4:5]
	v_fma_f32 v27, -v23, v26, v25
	v_mul_f32_e32 v14, 0x37800000, v13
	v_fmac_f32_e32 v26, v27, v24
	s_waitcnt lgkmcnt(0)
	v_add_f32_e32 v10, v10, v11
	ds_bpermute_b32 v11, v194, v10
	v_cndmask_b32_e64 v13, v13, v14, s[0:1]
	v_cmp_class_f32_e64 s[0:1], v30, v171
	v_fma_f32 v12, -v23, v26, v25
	v_div_fmas_f32 v12, v12, v24, v26
	s_waitcnt lgkmcnt(0)
	v_add_f32_e32 v10, v10, v11
	ds_bpermute_b32 v11, v197, v10
	v_cndmask_b32_e64 v25, v13, v30, s[0:1]
	v_div_scale_f32 v27, s[0:1], v25, v25, 1.0
	v_rcp_f32_e32 v30, v27
	s_waitcnt lgkmcnt(0)
	v_add_f32_e32 v10, v10, v11
	ds_bpermute_b32 v11, v198, v10
	v_div_fixup_f32 v130, v12, v22, 1.0
	v_fma_f32 v12, -v27, v30, 1.0
	v_fmac_f32_e32 v30, v12, v30
	v_mov_b32_e32 v12, v39
	s_waitcnt lgkmcnt(0)
; __device__ __forceinline__ void ph9_router(const Frame& F, const Args& A) {
;     ...
;         float rstd[4];
; #pragma unroll
;         for (int r = 0; r < 4; ++r) { float ss = 0.f;
; #pragma unroll
;             for (int j = 0; j < 8; ++j) ss += (hv[r][j].x * hv[r][j].x + hv[r][j].y * hv[r][j].y) + (hv[r][j].z * hv[r][j].z + hv[r][j].w * hv[r][j].w);
;             rstd[r] = 1.f / sqrtf(wave_sum(ss) * (1.f / DM) + EPS_); }
; #pragma unroll
;         for (int j = 0; j < 8; ++j) { const int col = 4 * lane + 256 * j;
;             const f32x4 g = *(const f32x4*)(g2n + col), sh = *(const f32x4*)(MOD + 6144 + col), sc = *(const f32x4*)(MOD + 8192 + col);
	v_add_f32_e32 v10, v10, v11
	v_fmamk_f32 v10, v10, 0x3a000000, v169
	v_mul_f32_e32 v11, 0x4f800000, v10
	v_cmp_gt_f32_e64 s[4:5], s47, v10
	v_mov_b32_e32 v13, v33
	v_pk_mul_f32 v[12:13], v[12:13], v[12:13]
	v_cndmask_b32_e64 v48, v10, v11, s[4:5]
	v_mov_b32_e32 v10, v38
	v_mov_b32_e32 v11, v32
	v_mov_b32_e32 v14, v41
	v_mov_b32_e32 v15, v29
	v_pk_fma_f32 v[10:11], v[10:11], v[10:11], v[12:13]
	v_mov_b32_e32 v12, v40
	v_mov_b32_e32 v13, v28
	v_pk_mul_f32 v[14:15], v[14:15], v[14:15]
	v_mul_f32_e32 v16, v61, v61
	v_pk_fma_f32 v[12:13], v[12:13], v[12:13], v[14:15]
	v_mov_b32_e32 v14, v35
	v_mov_b32_e32 v15, v37
	v_pk_add_f32 v[10:11], v[10:11], v[12:13]
	v_mov_b32_e32 v12, v34
	v_mov_b32_e32 v13, v36
	v_pk_mul_f32 v[14:15], v[14:15], v[14:15]
	v_pk_add_f32 v[10:11], v[10:11], v[10:11] op_sel:[0,1] op_sel_hi:[1,0]
	v_pk_fma_f32 v[12:13], v[12:13], v[12:13], v[14:15]
	v_mul_f32_e32 v14, v47, v47
	v_pk_add_f32 v[12:13], v[12:13], v[12:13] op_sel:[0,1] op_sel_hi:[1,0]
	v_pk_fma_f32 v[14:15], v[46:47], v[46:47], v[14:15] op_sel_hi:[1,1,0]
	v_pk_fma_f32 v[16:17], v[60:61], v[60:61], v[16:17] op_sel_hi:[1,1,0]
	v_pk_mul_f32 v[18:19], v[74:75], v[74:75]
	v_pk_mul_f32 v[20:21], v[164:165], v[164:165]
	v_mov_b32_e32 v11, v18
	v_mov_b32_e32 v13, v19
	v_mov_b32_e32 v15, v20
	v_mov_b32_e32 v17, v21
	v_pk_add_f32 v[10:11], v[10:11], v[12:13]
	v_pk_add_f32 v[12:13], v[14:15], v[16:17]
	v_mov_b32_e32 v14, v153
	v_mov_b32_e32 v15, v167
	v_pk_add_f32 v[10:11], v[10:11], v[12:13]
	v_mov_b32_e32 v12, v152
	v_mov_b32_e32 v13, v166
	v_pk_mul_f32 v[14:15], v[14:15], v[14:15]
	v_pk_add_f32 v[10:11], v[10:11], v[10:11] op_sel:[0,1] op_sel_hi:[1,0]
	v_pk_fma_f32 v[12:13], v[12:13], v[12:13], v[14:15]
	v_mul_f32_e32 v14, v7, v7
	v_pk_fma_f32 v[18:19], v[6:7], v[6:7], v[14:15] op_sel_hi:[1,1,0]
	v_mul_f32_e32 v14, v9, v9
	v_pk_add_f32 v[12:13], v[12:13], v[12:13] op_sel:[0,1] op_sel_hi:[1,0]
	v_pk_fma_f32 v[20:21], v[8:9], v[8:9], v[14:15] op_sel_hi:[1,1,0]
	v_pk_mul_f32 v[14:15], v[2:3], v[2:3]
	v_pk_mul_f32 v[16:17], v[4:5], v[4:5]
	v_mov_b32_e32 v11, v14
	v_mov_b32_e32 v13, v15
	v_pk_add_f32 v[22:23], v[10:11], v[12:13]
	v_lshlrev_b32_e32 v10, 2, v132
	v_ashrrev_i32_e32 v11, 31, v10
	v_lshlrev_b64 v[14:15], 2, v[10:11]
	v_lshl_add_u64 v[174:175], s[34:35], 0, v[14:15]
	v_lshl_add_u64 v[176:177], s[36:37], 0, v[14:15]
	global_load_dwordx4 v[42:45], v[174:175], off
	global_load_dwordx4 v[10:13], v[176:177], off
	v_lshl_add_u64 v[178:179], s[70:71], 0, v[14:15]
	v_mov_b32_e32 v19, v16
	v_mov_b32_e32 v21, v17
	global_load_dwordx4 v[14:17], v[178:179], off
	s_movk_i32 s98, 0x1000
	s_mov_b32 s99, 0
	global_load_dwordx4 v[200:203], v[176:177], off offset:1024
	global_load_dwordx4 v[204:207], v[178:179], off offset:1024
	global_load_dwordx4 v[208:211], v[174:175], off offset:1024
	global_load_dwordx4 v[212:215], v[176:177], off offset:2048
	global_load_dwordx4 v[216:219], v[178:179], off offset:2048
	global_load_dwordx4 v[220:223], v[174:175], off offset:2048
	global_load_dwordx4 v[224:227], v[176:177], off offset:3072
	global_load_dwordx4 v[228:231], v[178:179], off offset:3072
	global_load_dwordx4 v[232:235], v[174:175], off offset:3072
	v_lshl_add_u64 v[248:249], v[178:179], 0, s[98:99]
	v_lshl_add_u64 v[250:251], v[176:177], 0, s[98:99]
	v_lshl_add_u64 v[252:253], v[174:175], 0, s[98:99]
	global_load_dwordx4 v[236:239], v[248:249], off
	global_load_dwordx4 v[240:243], v[250:251], off
	global_load_dwordx4 v[244:247], v[252:253], off
	v_pk_add_f32 v[18:19], v[18:19], v[20:21]
	v_sqrt_f32_e32 v49, v48
	v_pk_add_f32 v[18:19], v[22:23], v[18:19]
	v_div_scale_f32 v24, vcc, 1.0, v25, 1.0
	v_add_f32_e32 v18, v18, v19
	ds_bpermute_b32 v19, v193, v18
	v_add_u32_e32 v21, -1, v49
	v_fma_f32 v22, -v21, v49, v48
	v_cmp_ge_f32_e64 s[0:1], 0, v22
	v_add_u32_e32 v22, 1, v49
	s_waitcnt lgkmcnt(0)
	v_add_f32_e32 v18, v18, v19
	ds_bpermute_b32 v19, v196, v18
	v_fma_f32 v23, -v22, v49, v48
	v_cndmask_b32_e64 v21, v49, v21, s[0:1]
	v_cmp_lt_f32_e64 s[0:1], 0, v23
	v_mul_f32_e32 v26, v24, v30
	s_waitcnt lgkmcnt(0)
	v_add_f32_e32 v18, v18, v19
	ds_bpermute_b32 v19, v195, v18
	v_cndmask_b32_e64 v21, v21, v22, s[0:1]
	v_mul_f32_e32 v22, 0x37800000, v21
	v_cndmask_b32_e64 v21, v21, v22, s[4:5]
	v_cmp_class_f32_e64 s[0:1], v48, v171
	s_waitcnt lgkmcnt(0)
	v_add_f32_e32 v18, v18, v19
	ds_bpermute_b32 v19, v194, v18
	v_cndmask_b32_e64 v21, v21, v48, s[0:1]
	v_div_scale_f32 v22, s[0:1], v21, v21, 1.0
	v_fma_f32 v31, -v27, v26, v24
	s_waitcnt lgkmcnt(0)
	v_add_f32_e32 v18, v18, v19
	ds_bpermute_b32 v19, v197, v18
	v_rcp_f32_e32 v23, v22
	v_fmac_f32_e32 v26, v31, v30
	v_fma_f32 v20, -v27, v26, v24
	v_div_fmas_f32 v20, v20, v30, v26
	s_waitcnt lgkmcnt(0)
	v_add_f32_e32 v18, v18, v19
	ds_bpermute_b32 v19, v198, v18
	v_div_fixup_f32 v168, v20, v25, 1.0
	v_fma_f32 v20, -v22, v23, 1.0
	v_fmac_f32_e32 v23, v20, v23
	v_div_scale_f32 v20, vcc, 1.0, v21, 1.0
	s_waitcnt lgkmcnt(0)
	v_add_f32_e32 v18, v18, v19
	v_fmamk_f32 v18, v18, 0x3a000000, v169
	v_mul_f32_e32 v19, 0x4f800000, v18
	v_cmp_gt_f32_e64 s[0:1], s47, v18
	v_mul_f32_e32 v24, v20, v23
	v_fma_f32 v25, -v22, v24, v20
	v_cndmask_b32_e64 v18, v18, v19, s[0:1]
	v_sqrt_f32_e32 v19, v18
	v_fmac_f32_e32 v24, v25, v23
	v_fma_f32 v20, -v22, v24, v20
	v_div_fmas_f32 v20, v20, v23, v24
	v_add_u32_e32 v22, -1, v19
	v_fma_f32 v25, -v22, v19, v18
	v_cmp_ge_f32_e64 s[4:5], 0, v25
	v_add_u32_e32 v25, 1, v19
	v_div_fixup_f32 v170, v20, v21, 1.0
	v_cndmask_b32_e64 v22, v19, v22, s[4:5]
	v_fma_f32 v19, -v25, v19, v18
	v_cmp_lt_f32_e64 s[4:5], 0, v19
	s_waitcnt vmcnt(13)
; __device__ __forceinline__ void ph9_router(const Frame& F, const Args& A) {
;     ...
;             rstd[r] = 1.f / sqrtf(wave_sum(ss) * (1.f / DM) + EPS_); }
; #pragma unroll
;         for (int j = 0; j < 8; ++j) { const int col = 4 * lane + 256 * j;
;             const f32x4 g = *(const f32x4*)(g2n + col), sh = *(const f32x4*)(MOD + 6144 + col), sc = *(const f32x4*)(MOD + 8192 + col);
;             const f32x4 gs1 = g * (sc + 1.f);
; #pragma unroll
;             for (int r = 0; r < 4; ++r) hv[r][j] = hv[r][j] * rstd[r] * gs1 + sh;
;             __builtin_amdgcn_sched_barrier(0); }
	v_pk_add_f32 v[10:11], v[10:11], 1.0 op_sel_hi:[1,0]
	v_cndmask_b32_e64 v19, v22, v25, s[4:5]
	v_mul_f32_e32 v22, 0x37800000, v19
	v_cndmask_b32_e64 v19, v19, v22, s[0:1]
	v_cmp_class_f32_e64 s[0:1], v18, v171
	v_pk_add_f32 v[12:13], v[12:13], 1.0 op_sel_hi:[1,0]
	s_nop 0
	v_cndmask_b32_e64 v18, v19, v18, s[0:1]
	v_div_scale_f32 v19, s[0:1], v18, v18, 1.0
	v_rcp_f32_e32 v22, v19
	s_waitcnt vmcnt(12)
	v_pk_mul_f32 v[12:13], v[16:17], v[12:13]
	v_fma_f32 v20, -v19, v22, 1.0
	v_fmac_f32_e32 v22, v20, v22
	v_div_scale_f32 v20, vcc, 1.0, v18, 1.0
	v_mul_f32_e32 v21, v20, v22
	v_fma_f32 v23, -v19, v21, v20
	v_fmac_f32_e32 v21, v23, v22
	v_fma_f32 v19, -v19, v21, v20
	v_div_fmas_f32 v19, v19, v22, v21
	v_div_fixup_f32 v172, v19, v18, 1.0
	v_pk_mul_f32 v[18:19], v[14:15], v[10:11]
	v_pk_mul_f32 v[10:11], v[156:157], v[130:131] op_sel_hi:[1,0]
	v_pk_mul_f32 v[14:15], v[158:159], v[130:131] op_sel_hi:[1,0]
	v_pk_fma_f32 v[30:31], v[10:11], v[18:19], v[42:43]
	v_pk_mul_f32 v[10:11], v[160:161], v[168:169] op_sel_hi:[1,0]
	v_pk_fma_f32 v[26:27], v[14:15], v[12:13], v[44:45]
	v_pk_mul_f32 v[14:15], v[162:163], v[168:169] op_sel_hi:[1,0]
	v_pk_fma_f32 v[24:25], v[10:11], v[18:19], v[42:43]
	v_pk_mul_f32 v[10:11], v[72:73], v[170:171] op_sel_hi:[1,0]
	v_pk_fma_f32 v[20:21], v[14:15], v[12:13], v[44:45]
	v_pk_mul_f32 v[14:15], v[68:69], v[170:171] op_sel_hi:[1,0]
	v_pk_fma_f32 v[16:17], v[10:11], v[18:19], v[42:43]
	v_pk_mul_f32 v[22:23], v[38:39], v[172:173] op_sel_hi:[1,0]
	v_pk_mul_f32 v[10:11], v[40:41], v[172:173] op_sel_hi:[1,0]
	v_pk_fma_f32 v[14:15], v[14:15], v[12:13], v[44:45]
	v_pk_fma_f32 v[10:11], v[12:13], v[10:11], v[44:45]
	v_pk_fma_f32 v[12:13], v[18:19], v[22:23], v[42:43]
	s_waitcnt vmcnt(9)
	v_mov_b64_e32 v[38:39], v[200:201]
	v_mov_b64_e32 v[40:41], v[202:203]
	v_mov_b64_e32 v[42:43], v[204:205]
	v_mov_b64_e32 v[44:45], v[206:207]
	v_mov_b64_e32 v[156:157], v[208:209]
	v_mov_b64_e32 v[158:159], v[210:211]
	global_load_dwordx4 v[200:203], v[250:251], off offset:1024
	global_load_dwordx4 v[204:207], v[248:249], off offset:1024
	global_load_dwordx4 v[208:211], v[252:253], off offset:1024
	v_pk_mul_f32 v[76:77], v[32:33], v[172:173] op_sel_hi:[1,0]
	v_pk_mul_f32 v[80:81], v[28:29], v[172:173] op_sel_hi:[1,0]
	v_pk_mul_f32 v[18:19], v[146:147], v[130:131] op_sel_hi:[1,0]
	v_pk_mul_f32 v[22:23], v[148:149], v[130:131] op_sel_hi:[1,0]
	v_pk_mul_f32 v[68:69], v[150:151], v[168:169] op_sel_hi:[1,0]
	v_pk_mul_f32 v[72:73], v[154:155], v[168:169] op_sel_hi:[1,0]
	v_pk_mul_f32 v[62:63], v[62:63], v[170:171] op_sel_hi:[1,0]
	v_pk_mul_f32 v[64:65], v[64:65], v[170:171] op_sel_hi:[1,0]
	v_pk_add_f32 v[28:29], v[40:41], 1.0 op_sel_hi:[1,0]
	v_pk_add_f32 v[32:33], v[38:39], 1.0 op_sel_hi:[1,0]
	v_pk_mul_f32 v[44:45], v[44:45], v[28:29]
	v_pk_mul_f32 v[42:43], v[42:43], v[32:33]
	v_pk_fma_f32 v[48:49], v[22:23], v[44:45], v[158:159]
	v_pk_fma_f32 v[52:53], v[18:19], v[42:43], v[156:157]
	v_pk_fma_f32 v[38:39], v[72:73], v[44:45], v[158:159]
	v_pk_fma_f32 v[40:41], v[68:69], v[42:43], v[156:157]
	v_pk_fma_f32 v[28:29], v[64:65], v[44:45], v[158:159]
	v_pk_fma_f32 v[32:33], v[62:63], v[42:43], v[156:157]
	v_pk_fma_f32 v[18:19], v[80:81], v[44:45], v[158:159]
	v_pk_fma_f32 v[22:23], v[76:77], v[42:43], v[156:157]
	s_waitcnt vmcnt(9)
	v_mov_b64_e32 v[42:43], v[212:213]
	v_mov_b64_e32 v[44:45], v[214:215]
	v_mov_b64_e32 v[62:63], v[216:217]
	v_mov_b64_e32 v[64:65], v[218:219]
	v_mov_b64_e32 v[146:147], v[220:221]
	v_mov_b64_e32 v[148:149], v[222:223]
	global_load_dwordx4 v[212:215], v[250:251], off offset:2048
	global_load_dwordx4 v[216:219], v[248:249], off offset:2048
	global_load_dwordx4 v[220:223], v[252:253], off offset:2048
	v_pk_mul_f32 v[72:73], v[142:143], v[130:131] op_sel_hi:[1,0]
	v_pk_mul_f32 v[142:143], v[34:35], v[172:173] op_sel_hi:[1,0]
	v_pk_mul_f32 v[34:35], v[36:37], v[172:173] op_sel_hi:[1,0]
	v_pk_mul_f32 v[68:69], v[140:141], v[130:131] op_sel_hi:[1,0]
	v_pk_mul_f32 v[76:77], v[128:129], v[168:169] op_sel_hi:[1,0]
	v_pk_mul_f32 v[80:81], v[144:145], v[168:169] op_sel_hi:[1,0]
	v_pk_mul_f32 v[128:129], v[54:55], v[170:171] op_sel_hi:[1,0]
	v_pk_mul_f32 v[140:141], v[56:57], v[170:171] op_sel_hi:[1,0]
	v_pk_add_f32 v[36:37], v[44:45], 1.0 op_sel_hi:[1,0]
	v_pk_add_f32 v[42:43], v[42:43], 1.0 op_sel_hi:[1,0]
	v_pk_mul_f32 v[36:37], v[64:65], v[36:37]
	v_pk_mul_f32 v[144:145], v[62:63], v[42:43]
	v_pk_fma_f32 v[62:63], v[72:73], v[36:37], v[148:149]
	v_pk_fma_f32 v[64:65], v[68:69], v[144:145], v[146:147]
	v_pk_fma_f32 v[54:55], v[80:81], v[36:37], v[148:149]
	v_pk_fma_f32 v[56:57], v[76:77], v[144:145], v[146:147]
	v_pk_fma_f32 v[42:43], v[140:141], v[36:37], v[148:149]
	v_pk_fma_f32 v[44:45], v[128:129], v[144:145], v[146:147]
	v_pk_fma_f32 v[34:35], v[34:35], v[36:37], v[148:149]
	v_pk_fma_f32 v[36:37], v[142:143], v[144:145], v[146:147]
	s_waitcnt vmcnt(9)
; __device__ __forceinline__ void ph9_router(const Frame& F, const Args& A) {
;     ...
;         for (int j = 0; j < 8; ++j) { const int col = 4 * lane + 256 * j;
;             const f32x4 g = *(const f32x4*)(g2n + col), sh = *(const f32x4*)(MOD + 6144 + col), sc = *(const f32x4*)(MOD + 8192 + col);
;             const f32x4 gs1 = g * (sc + 1.f);
; #pragma unroll
;             for (int r = 0; r < 4; ++r) hv[r][j] = hv[r][j] * rstd[r] * gs1 + sh;
;             __builtin_amdgcn_sched_barrier(0); }
	v_mov_b64_e32 v[140:141], v[224:225]
	v_mov_b64_e32 v[142:143], v[226:227]
	v_mov_b64_e32 v[144:145], v[228:229]
	v_mov_b64_e32 v[146:147], v[230:231]
	v_mov_b64_e32 v[148:149], v[232:233]
	v_mov_b64_e32 v[150:151], v[234:235]
	global_load_dwordx4 v[224:227], v[250:251], off offset:3072
	global_load_dwordx4 v[228:231], v[248:249], off offset:3072
	global_load_dwordx4 v[232:235], v[252:253], off offset:3072
	v_pk_mul_f32 v[68:69], v[104:105], v[130:131] op_sel_hi:[1,0]
	v_pk_mul_f32 v[104:105], v[46:47], v[172:173] op_sel_hi:[1,0]
	v_pk_mul_f32 v[46:47], v[60:61], v[172:173] op_sel_hi:[1,0]
	v_pk_mul_f32 v[72:73], v[116:117], v[130:131] op_sel_hi:[1,0]
	v_pk_mul_f32 v[86:87], v[86:87], v[168:169] op_sel_hi:[1,0]
	v_pk_mul_f32 v[88:89], v[88:89], v[168:169] op_sel_hi:[1,0]
	v_pk_mul_f32 v[50:51], v[50:51], v[170:171] op_sel_hi:[1,0]
	v_pk_mul_f32 v[58:59], v[58:59], v[170:171] op_sel_hi:[1,0]
	v_pk_add_f32 v[60:61], v[142:143], 1.0 op_sel_hi:[1,0]
	v_pk_add_f32 v[76:77], v[140:141], 1.0 op_sel_hi:[1,0]
	v_pk_mul_f32 v[116:117], v[146:147], v[60:61]
	v_pk_mul_f32 v[128:129], v[144:145], v[76:77]
	v_pk_fma_f32 v[76:77], v[72:73], v[116:117], v[150:151]
	v_pk_fma_f32 v[80:81], v[68:69], v[128:129], v[148:149]
	v_pk_fma_f32 v[68:69], v[88:89], v[116:117], v[150:151]
	v_pk_fma_f32 v[72:73], v[86:87], v[128:129], v[148:149]
	v_pk_fma_f32 v[58:59], v[58:59], v[116:117], v[150:151]
	v_pk_fma_f32 v[60:61], v[50:51], v[128:129], v[148:149]
	v_pk_fma_f32 v[46:47], v[46:47], v[116:117], v[150:151]
	v_pk_fma_f32 v[50:51], v[104:105], v[128:129], v[148:149]
	v_add_co_u32_e32 v148, vcc, s46, v178
	v_pk_mul_f32 v[104:105], v[96:97], v[130:131] op_sel_hi:[1,0]
	s_nop 0
	v_addc_co_u32_e32 v149, vcc, 0, v179, vcc
	v_add_co_u32_e32 v150, vcc, s46, v176
	s_waitcnt vmcnt(9)
	v_mov_b64_e32 v[86:87], v[236:237]
	v_mov_b64_e32 v[88:89], v[238:239]
	s_nop 0
	v_addc_co_u32_e32 v151, vcc, 0, v177, vcc
	v_mov_b64_e32 v[140:141], v[240:241]
	v_mov_b64_e32 v[142:143], v[242:243]
	v_add_co_u32_e32 v154, vcc, s46, v174
	v_pk_mul_f32 v[96:97], v[102:103], v[130:131] op_sel_hi:[1,0]
	s_nop 0
	v_addc_co_u32_e32 v155, vcc, 0, v175, vcc
	v_mov_b64_e32 v[144:145], v[244:245]
	v_mov_b64_e32 v[146:147], v[246:247]
	v_pk_mul_f32 v[102:103], v[100:101], v[168:169] op_sel_hi:[1,0]
	v_pk_mul_f32 v[116:117], v[74:75], v[172:173] op_sel_hi:[1,0]
	v_pk_mul_f32 v[78:79], v[78:79], v[168:169] op_sel_hi:[1,0]
	v_pk_mul_f32 v[66:67], v[66:67], v[170:171] op_sel_hi:[1,0]
	v_pk_mul_f32 v[70:71], v[70:71], v[170:171] op_sel_hi:[1,0]
	v_pk_mul_f32 v[128:129], v[164:165], v[172:173] op_sel_hi:[1,0]
	v_pk_add_f32 v[74:75], v[142:143], 1.0 op_sel_hi:[1,0]
	v_pk_add_f32 v[100:101], v[140:141], 1.0 op_sel_hi:[1,0]
	v_pk_mul_f32 v[140:141], v[88:89], v[74:75]
	v_pk_mul_f32 v[142:143], v[86:87], v[100:101]
	v_pk_fma_f32 v[96:97], v[96:97], v[140:141], v[146:147]
	v_pk_fma_f32 v[100:101], v[104:105], v[142:143], v[144:145]
	v_pk_fma_f32 v[86:87], v[102:103], v[140:141], v[146:147]
	v_pk_fma_f32 v[88:89], v[78:79], v[142:143], v[144:145]
	v_pk_fma_f32 v[74:75], v[70:71], v[140:141], v[146:147]
	v_pk_fma_f32 v[78:79], v[66:67], v[142:143], v[144:145]
	v_pk_fma_f32 v[66:67], v[128:129], v[140:141], v[146:147]
	v_pk_fma_f32 v[70:71], v[116:117], v[142:143], v[144:145]
	s_waitcnt vmcnt(6)
; __device__ __forceinline__ void ph9_router(const Frame& F, const Args& A) {
;     ...
;         for (int j = 0; j < 8; ++j) { const int col = 4 * lane + 256 * j;
;             const f32x4 g = *(const f32x4*)(g2n + col), sh = *(const f32x4*)(MOD + 6144 + col), sc = *(const f32x4*)(MOD + 8192 + col);
;             const f32x4 gs1 = g * (sc + 1.f);
; #pragma unroll
;             for (int r = 0; r < 4; ++r) hv[r][j] = hv[r][j] * rstd[r] * gs1 + sh;
;             __builtin_amdgcn_sched_barrier(0); }
;         float lgv[2];
; #pragma unroll 1
;         for (int half = 0; half < 2; ++half) {
;             if (half == 1) { __syncthreads();
;               const f32x4* src = (const f32x4*)(WRT + (size_t)16 * DM);
; #pragma unroll 1
;               for (int i0 = 0; i0 < 16; i0 += 8) { f32x4 t8[8];
; #pragma unroll
;                 for (int i = 0; i < 8; ++i) t8[i] = src[tid + 512 * (i0 + i)];
; #pragma unroll
;                 for (int i = 0; i < 8; ++i) wl[tid + 512 * (i0 + i)] = t8[i]; } }
;             __syncthreads();
;             float mine = 0.f;
;             const bool b0 = lane & 1, b1 = lane & 2, b4 = lane & 16, b5 = lane & 32;
	v_mov_b64_e32 v[102:103], v[200:201]
	v_mov_b64_e32 v[104:105], v[202:203]
	v_mov_b64_e32 v[140:141], v[204:205]
	v_mov_b64_e32 v[142:143], v[206:207]
	v_mov_b64_e32 v[144:145], v[208:209]
	v_mov_b64_e32 v[146:147], v[210:211]
	v_pk_mul_f32 v[90:91], v[90:91], v[130:131] op_sel_hi:[1,0]
	v_pk_mul_f32 v[92:93], v[92:93], v[130:131] op_sel_hi:[1,0]
	v_pk_mul_f32 v[82:83], v[82:83], v[168:169] op_sel_hi:[1,0]
	v_pk_mul_f32 v[84:85], v[84:85], v[168:169] op_sel_hi:[1,0]
	v_pk_mul_f32 v[128:129], v[112:113], v[170:171] op_sel_hi:[1,0]
	v_pk_mul_f32 v[126:127], v[126:127], v[170:171] op_sel_hi:[1,0]
	v_pk_mul_f32 v[152:153], v[152:153], v[172:173] op_sel_hi:[1,0]
	v_pk_mul_f32 v[156:157], v[166:167], v[172:173] op_sel_hi:[1,0]
	v_pk_add_f32 v[104:105], v[104:105], 1.0 op_sel_hi:[1,0]
	v_pk_add_f32 v[102:103], v[102:103], 1.0 op_sel_hi:[1,0]
	v_pk_mul_f32 v[142:143], v[142:143], v[104:105]
	v_pk_mul_f32 v[140:141], v[140:141], v[102:103]
	v_pk_fma_f32 v[112:113], v[92:93], v[142:143], v[146:147]
	v_pk_fma_f32 v[116:117], v[90:91], v[140:141], v[144:145]
	v_pk_fma_f32 v[102:103], v[84:85], v[142:143], v[146:147]
	v_pk_fma_f32 v[104:105], v[82:83], v[140:141], v[144:145]
	v_pk_fma_f32 v[90:91], v[126:127], v[142:143], v[146:147]
	v_pk_fma_f32 v[92:93], v[128:129], v[140:141], v[144:145]
	v_pk_fma_f32 v[82:83], v[156:157], v[142:143], v[146:147]
	v_pk_fma_f32 v[84:85], v[152:153], v[140:141], v[144:145]
	s_waitcnt vmcnt(3)
	v_mov_b64_e32 v[126:127], v[212:213]
	v_mov_b64_e32 v[128:129], v[214:215]
	v_mov_b64_e32 v[140:141], v[216:217]
	v_mov_b64_e32 v[142:143], v[218:219]
	v_mov_b64_e32 v[144:145], v[220:221]
	v_mov_b64_e32 v[146:147], v[222:223]
	v_pk_mul_f32 v[152:153], v[118:119], v[170:171] op_sel_hi:[1,0]
	v_pk_mul_f32 v[156:157], v[120:121], v[170:171] op_sel_hi:[1,0]
	v_pk_mul_f32 v[94:95], v[94:95], v[130:131] op_sel_hi:[1,0]
	v_pk_mul_f32 v[106:107], v[106:107], v[130:131] op_sel_hi:[1,0]
	v_pk_mul_f32 v[98:99], v[98:99], v[168:169] op_sel_hi:[1,0]
	v_pk_mul_f32 v[108:109], v[108:109], v[168:169] op_sel_hi:[1,0]
	v_pk_mul_f32 v[6:7], v[6:7], v[172:173] op_sel_hi:[1,0]
	v_pk_mul_f32 v[8:9], v[8:9], v[172:173] op_sel_hi:[1,0]
	v_pk_add_f32 v[118:119], v[128:129], 1.0 op_sel_hi:[1,0]
	v_pk_add_f32 v[120:121], v[126:127], 1.0 op_sel_hi:[1,0]
	v_pk_mul_f32 v[142:143], v[142:143], v[118:119]
	v_pk_mul_f32 v[140:141], v[140:141], v[120:121]
	v_pk_fma_f32 v[126:127], v[106:107], v[142:143], v[146:147]
	v_pk_fma_f32 v[128:129], v[94:95], v[140:141], v[144:145]
	v_pk_fma_f32 v[118:119], v[108:109], v[142:143], v[146:147]
	v_pk_fma_f32 v[120:121], v[98:99], v[140:141], v[144:145]
	v_pk_fma_f32 v[106:107], v[156:157], v[142:143], v[146:147]
	v_pk_fma_f32 v[108:109], v[152:153], v[140:141], v[144:145]
	v_pk_fma_f32 v[94:95], v[8:9], v[142:143], v[146:147]
	v_pk_fma_f32 v[98:99], v[6:7], v[140:141], v[144:145]
	s_waitcnt vmcnt(0)
	v_mov_b64_e32 v[6:7], v[224:225]
	v_mov_b64_e32 v[8:9], v[226:227]
	v_mov_b64_e32 v[140:141], v[228:229]
	v_mov_b64_e32 v[142:143], v[230:231]
	v_mov_b64_e32 v[144:145], v[232:233]
	v_mov_b64_e32 v[146:147], v[234:235]
	v_pk_mul_f32 v[114:115], v[114:115], v[130:131] op_sel_hi:[1,0]
	v_pk_mul_f32 v[122:123], v[122:123], v[130:131] op_sel_hi:[1,0]
	v_pk_mul_f32 v[110:111], v[110:111], v[168:169] op_sel_hi:[1,0]
	v_pk_mul_f32 v[124:125], v[124:125], v[168:169] op_sel_hi:[1,0]
	v_pk_mul_f32 v[148:149], v[136:137], v[170:171] op_sel_hi:[1,0]
	v_pk_mul_f32 v[150:151], v[138:139], v[170:171] op_sel_hi:[1,0]
	v_pk_mul_f32 v[2:3], v[2:3], v[172:173] op_sel_hi:[1,0]
	v_pk_mul_f32 v[4:5], v[4:5], v[172:173] op_sel_hi:[1,0]
	v_pk_add_f32 v[8:9], v[8:9], 1.0 op_sel_hi:[1,0]
	v_pk_add_f32 v[6:7], v[6:7], 1.0 op_sel_hi:[1,0]
	v_pk_mul_f32 v[8:9], v[142:143], v[8:9]
	v_pk_mul_f32 v[6:7], v[140:141], v[6:7]
	v_pk_fma_f32 v[140:141], v[122:123], v[8:9], v[146:147]
	v_pk_fma_f32 v[142:143], v[114:115], v[6:7], v[144:145]
	v_pk_fma_f32 v[136:137], v[124:125], v[8:9], v[146:147]
	v_pk_fma_f32 v[138:139], v[110:111], v[6:7], v[144:145]
	v_pk_fma_f32 v[122:123], v[150:151], v[8:9], v[146:147]
	v_pk_fma_f32 v[124:125], v[148:149], v[6:7], v[144:145]
	v_pk_fma_f32 v[110:111], v[4:5], v[8:9], v[146:147]
	v_pk_fma_f32 v[114:115], v[2:3], v[6:7], v[144:145]
	v_and_b32_e32 v2, 1, v132
	v_cmp_eq_u32_e64 s[4:5], 0, v2
	v_and_b32_e32 v2, 2, v132
	v_cmp_eq_u32_e64 s[6:7], 0, v2
	v_and_b32_e32 v2, 16, v132
	v_cmp_eq_u32_e64 s[8:9], 0, v2
	v_and_b32_e32 v2, 32, v132
	v_cmp_eq_u32_e64 s[10:11], 0, v2
	v_lshlrev_b32_e32 v2, 13, v132
	v_lshl_add_u32 v157, v132, 4, 0
	v_and_b32_e32 v156, 15, v132
	v_and_b32_e32 v158, 0x18000, v2
	s_mov_b64 s[0:1], -1
	s_mov_b64 s[12:13], 0
	s_cbranch_execnz .LBB0_1198

; __device__ __forceinline__ void ph9_router(const Frame& F, const Args& A) {
;     ...
;             for (int g = 0; g < 4; ++g) { float q[4][4];
; #pragma unroll
;                 for (int el = 0; el < 4; ++el) { f32x4 a0 = {0.f, 0.f, 0.f, 0.f}, a1 = a0, a2 = a0, a3 = a0;
; #pragma unroll
;                     for (int j = 0; j < 8; ++j) { const f32x4 w = wl[(4 * g + el) * 512 + lane + 64 * j];
;                         a0 += hv[0][j] * w; a1 += hv[1][j] * w; a2 += hv[2][j] * w; a3 += hv[3][j] * w; }
;                     q[0][el] = (a0.x + a0.y) + (a0.z + a0.w); q[1][el] = (a1.x + a1.y) + (a1.z + a1.w); q[2][el] = (a2.x + a2.y) + (a2.z + a2.w); q[3][el] = (a3.x + a3.y) + (a3.z + a3.w); }
;                 float s1[2][4], s2[4], s3[2];
; #pragma unroll
;                 for (int k = 0; k < 2; ++k)
; #pragma unroll
;                     for (int el = 0; el < 4; ++el) { const float keep = b4 ? q[2 * k + 1][el] : q[2 * k][el], send = b4 ? q[2 * k][el] : q[2 * k + 1][el]; s1[k][el] = keep + __shfl_xor(send, 16); }
; #pragma unroll
;                 for (int el = 0; el < 4; ++el) { const float keep = b5 ? s1[1][el] : s1[0][el], send = b5 ? s1[0][el] : s1[1][el]; s2[el] = keep + __shfl_xor(send, 32); }
; #pragma unroll
;                 for (int k = 0; k < 2; ++k) { const float keep = b0 ? s2[2 * k + 1] : s2[2 * k], send = b0 ? s2[2 * k] : s2[2 * k + 1]; s3[k] = keep + __shfl_xor(send, 1); }
;                 float s4; { const float keep = b1 ? s3[1] : s3[0], send = b1 ? s3[0] : s3[1]; s4 = keep + __shfl_xor(send, 2); }
;                 s4 += __shfl_xor(s4, 4); s4 += __shfl_xor(s4, 8);
;                 if (((lane >> 2) & 3) == g) mine = s4; }
.LBB0_1199:
	v_add_u32_e32 v2, s14, v157
	v_cmp_eq_u32_e32 vcc, s14, v158
	s_add_i32 s14, s14, 0x8000
	s_cmp_eq_u32 s14, 0x20000
	ds_read_b128 v[230:233], v2
	ds_read_b128 v[234:237], v2 offset:1024
	ds_read_b128 v[238:241], v2 offset:2048
	ds_read_b128 v[242:245], v2 offset:3072
	s_waitcnt lgkmcnt(3)
	v_pk_fma_f32 v[8:9], v[26:27], v[232:233], 0 op_sel_hi:[1,1,0]
	v_pk_fma_f32 v[144:145], v[30:31], v[230:231], 0 op_sel_hi:[1,1,0]
	v_pk_fma_f32 v[146:147], v[20:21], v[232:233], 0 op_sel_hi:[1,1,0]
	v_pk_fma_f32 v[148:149], v[24:25], v[230:231], 0 op_sel_hi:[1,1,0]
	v_pk_fma_f32 v[150:151], v[14:15], v[232:233], 0 op_sel_hi:[1,1,0]
	v_pk_fma_f32 v[152:153], v[16:17], v[230:231], 0 op_sel_hi:[1,1,0]
	v_pk_fma_f32 v[154:155], v[10:11], v[232:233], 0 op_sel_hi:[1,1,0]
	v_pk_fma_f32 v[160:161], v[12:13], v[230:231], 0 op_sel_hi:[1,1,0]
	ds_read_b128 v[230:233], v2 offset:4096
	s_waitcnt lgkmcnt(3)
	v_pk_fma_f32 v[8:9], v[48:49], v[236:237], v[8:9]
	v_pk_fma_f32 v[144:145], v[52:53], v[234:235], v[144:145]
	v_pk_fma_f32 v[146:147], v[38:39], v[236:237], v[146:147]
	v_pk_fma_f32 v[148:149], v[40:41], v[234:235], v[148:149]
	v_pk_fma_f32 v[150:151], v[28:29], v[236:237], v[150:151]
	v_pk_fma_f32 v[152:153], v[32:33], v[234:235], v[152:153]
	v_pk_fma_f32 v[154:155], v[18:19], v[236:237], v[154:155]
	v_pk_fma_f32 v[160:161], v[22:23], v[234:235], v[160:161]
	ds_read_b128 v[234:237], v2 offset:5120
	s_waitcnt lgkmcnt(3)
	v_pk_fma_f32 v[8:9], v[62:63], v[240:241], v[8:9]
	v_pk_fma_f32 v[144:145], v[64:65], v[238:239], v[144:145]
	v_pk_fma_f32 v[146:147], v[54:55], v[240:241], v[146:147]
	v_pk_fma_f32 v[148:149], v[56:57], v[238:239], v[148:149]
	v_pk_fma_f32 v[150:151], v[42:43], v[240:241], v[150:151]
	v_pk_fma_f32 v[152:153], v[44:45], v[238:239], v[152:153]
	v_pk_fma_f32 v[154:155], v[34:35], v[240:241], v[154:155]
	v_pk_fma_f32 v[160:161], v[36:37], v[238:239], v[160:161]
	ds_read_b128 v[238:241], v2 offset:6144
	s_waitcnt lgkmcnt(3)
	v_pk_fma_f32 v[8:9], v[76:77], v[244:245], v[8:9]
	v_pk_fma_f32 v[144:145], v[80:81], v[242:243], v[144:145]
	v_pk_fma_f32 v[146:147], v[68:69], v[244:245], v[146:147]
	v_pk_fma_f32 v[148:149], v[72:73], v[242:243], v[148:149]
	v_pk_fma_f32 v[150:151], v[58:59], v[244:245], v[150:151]
	v_pk_fma_f32 v[152:153], v[60:61], v[242:243], v[152:153]
	v_pk_fma_f32 v[154:155], v[46:47], v[244:245], v[154:155]
	v_pk_fma_f32 v[160:161], v[50:51], v[242:243], v[160:161]
	ds_read_b128 v[4:7], v2 offset:7168
	s_waitcnt lgkmcnt(3)
	v_pk_fma_f32 v[8:9], v[96:97], v[232:233], v[8:9]
	v_pk_fma_f32 v[144:145], v[100:101], v[230:231], v[144:145]
	v_pk_fma_f32 v[146:147], v[86:87], v[232:233], v[146:147]
	v_pk_fma_f32 v[148:149], v[88:89], v[230:231], v[148:149]
	v_pk_fma_f32 v[150:151], v[74:75], v[232:233], v[150:151]
	v_pk_fma_f32 v[152:153], v[78:79], v[230:231], v[152:153]
	v_pk_fma_f32 v[154:155], v[66:67], v[232:233], v[154:155]
	v_pk_fma_f32 v[160:161], v[70:71], v[230:231], v[160:161]
	ds_read_b128 v[230:233], v2 offset:8192
	s_waitcnt lgkmcnt(3)
	v_pk_fma_f32 v[8:9], v[112:113], v[236:237], v[8:9]
	v_pk_fma_f32 v[144:145], v[116:117], v[234:235], v[144:145]
	v_pk_fma_f32 v[146:147], v[102:103], v[236:237], v[146:147]
	v_pk_fma_f32 v[148:149], v[104:105], v[234:235], v[148:149]
	v_pk_fma_f32 v[150:151], v[90:91], v[236:237], v[150:151]
	v_pk_fma_f32 v[152:153], v[92:93], v[234:235], v[152:153]
	v_pk_fma_f32 v[154:155], v[82:83], v[236:237], v[154:155]
	v_pk_fma_f32 v[160:161], v[84:85], v[234:235], v[160:161]
	ds_read_b128 v[234:237], v2 offset:9216
	s_waitcnt lgkmcnt(3)
	v_pk_fma_f32 v[8:9], v[126:127], v[240:241], v[8:9]
	v_pk_fma_f32 v[144:145], v[128:129], v[238:239], v[144:145]
	v_pk_fma_f32 v[146:147], v[118:119], v[240:241], v[146:147]
	v_pk_fma_f32 v[148:149], v[120:121], v[238:239], v[148:149]
	v_pk_fma_f32 v[150:151], v[106:107], v[240:241], v[150:151]
	v_pk_fma_f32 v[152:153], v[108:109], v[238:239], v[152:153]
	v_pk_fma_f32 v[154:155], v[94:95], v[240:241], v[154:155]
	v_pk_fma_f32 v[160:161], v[98:99], v[238:239], v[160:161]
	ds_read_b128 v[238:241], v2 offset:10240
	s_waitcnt lgkmcnt(3)
	v_pk_fma_f32 v[8:9], v[140:141], v[6:7], v[8:9]
	v_pk_fma_f32 v[144:145], v[142:143], v[4:5], v[144:145]
	v_pk_fma_f32 v[146:147], v[136:137], v[6:7], v[146:147]
	v_pk_fma_f32 v[150:151], v[122:123], v[6:7], v[150:151]
	v_pk_fma_f32 v[6:7], v[110:111], v[6:7], v[154:155]
	v_pk_mov_b32 v[154:155], v[144:145], v[8:9] op_sel:[1,0]
	v_mov_b32_e32 v145, v9
	v_pk_fma_f32 v[148:149], v[138:139], v[4:5], v[148:149]
	v_pk_add_f32 v[8:9], v[154:155], v[144:145]
	v_pk_fma_f32 v[152:153], v[124:125], v[4:5], v[152:153]
	v_pk_fma_f32 v[4:5], v[114:115], v[4:5], v[160:161]
	v_add_f32_e32 v161, v8, v9
	v_pk_mov_b32 v[8:9], v[148:149], v[146:147] op_sel:[1,0]
	v_mov_b32_e32 v149, v147
	v_pk_add_f32 v[8:9], v[8:9], v[148:149]
	s_nop 0
	v_add_f32_e32 v162, v8, v9
	v_pk_mov_b32 v[8:9], v[152:153], v[150:151] op_sel:[1,0]
	v_mov_b32_e32 v153, v151
	v_pk_add_f32 v[8:9], v[8:9], v[152:153]
	s_nop 0
	v_add_f32_e32 v130, v8, v9
	v_pk_mov_b32 v[8:9], v[4:5], v[6:7] op_sel:[1,0]
	v_mov_b32_e32 v5, v7
	v_pk_add_f32 v[4:5], v[8:9], v[4:5]
	s_nop 0
	v_add_f32_e32 v160, v4, v5
	ds_read_b128 v[242:245], v2 offset:11264
	s_waitcnt lgkmcnt(3)
	v_pk_fma_f32 v[8:9], v[26:27], v[232:233], 0 op_sel_hi:[1,1,0]
	v_pk_fma_f32 v[144:145], v[30:31], v[230:231], 0 op_sel_hi:[1,1,0]
	v_pk_fma_f32 v[146:147], v[20:21], v[232:233], 0 op_sel_hi:[1,1,0]
	v_pk_fma_f32 v[148:149], v[24:25], v[230:231], 0 op_sel_hi:[1,1,0]
	v_pk_fma_f32 v[150:151], v[14:15], v[232:233], 0 op_sel_hi:[1,1,0]
	v_pk_fma_f32 v[152:153], v[16:17], v[230:231], 0 op_sel_hi:[1,1,0]
	v_pk_fma_f32 v[154:155], v[10:11], v[232:233], 0 op_sel_hi:[1,1,0]
	v_pk_fma_f32 v[164:165], v[12:13], v[230:231], 0 op_sel_hi:[1,1,0]
	ds_read_b128 v[230:233], v2 offset:12288
	s_waitcnt lgkmcnt(3)
; __device__ __forceinline__ void ph9_router(const Frame& F, const Args& A) {
;     ...
;             for (int g = 0; g < 4; ++g) { float q[4][4];
; #pragma unroll
;                 for (int el = 0; el < 4; ++el) { f32x4 a0 = {0.f, 0.f, 0.f, 0.f}, a1 = a0, a2 = a0, a3 = a0;
; #pragma unroll
;                     for (int j = 0; j < 8; ++j) { const f32x4 w = wl[(4 * g + el) * 512 + lane + 64 * j];
;                         a0 += hv[0][j] * w; a1 += hv[1][j] * w; a2 += hv[2][j] * w; a3 += hv[3][j] * w; }
;                     q[0][el] = (a0.x + a0.y) + (a0.z + a0.w); q[1][el] = (a1.x + a1.y) + (a1.z + a1.w); q[2][el] = (a2.x + a2.y) + (a2.z + a2.w); q[3][el] = (a3.x + a3.y) + (a3.z + a3.w); }
;                 float s1[2][4], s2[4], s3[2];
; #pragma unroll
;                 for (int k = 0; k < 2; ++k)
; #pragma unroll
;                     for (int el = 0; el < 4; ++el) { const float keep = b4 ? q[2 * k + 1][el] : q[2 * k][el], send = b4 ? q[2 * k][el] : q[2 * k + 1][el]; s1[k][el] = keep + __shfl_xor(send, 16); }
; #pragma unroll
;                 for (int el = 0; el < 4; ++el) { const float keep = b5 ? s1[1][el] : s1[0][el], send = b5 ? s1[0][el] : s1[1][el]; s2[el] = keep + __shfl_xor(send, 32); }
; #pragma unroll
;                 for (int k = 0; k < 2; ++k) { const float keep = b0 ? s2[2 * k + 1] : s2[2 * k], send = b0 ? s2[2 * k] : s2[2 * k + 1]; s3[k] = keep + __shfl_xor(send, 1); }
;                 float s4; { const float keep = b1 ? s3[1] : s3[0], send = b1 ? s3[0] : s3[1]; s4 = keep + __shfl_xor(send, 2); }
;                 s4 += __shfl_xor(s4, 4); s4 += __shfl_xor(s4, 8);
;                 if (((lane >> 2) & 3) == g) mine = s4; }
	v_pk_fma_f32 v[8:9], v[48:49], v[236:237], v[8:9]
	v_pk_fma_f32 v[144:145], v[52:53], v[234:235], v[144:145]
	v_pk_fma_f32 v[146:147], v[38:39], v[236:237], v[146:147]
	v_pk_fma_f32 v[148:149], v[40:41], v[234:235], v[148:149]
	v_pk_fma_f32 v[150:151], v[28:29], v[236:237], v[150:151]
	v_pk_fma_f32 v[152:153], v[32:33], v[234:235], v[152:153]
	v_pk_fma_f32 v[154:155], v[18:19], v[236:237], v[154:155]
	v_pk_fma_f32 v[164:165], v[22:23], v[234:235], v[164:165]
	ds_read_b128 v[234:237], v2 offset:13312
	s_waitcnt lgkmcnt(3)
	v_pk_fma_f32 v[8:9], v[62:63], v[240:241], v[8:9]
	v_pk_fma_f32 v[144:145], v[64:65], v[238:239], v[144:145]
	v_pk_fma_f32 v[146:147], v[54:55], v[240:241], v[146:147]
	v_pk_fma_f32 v[148:149], v[56:57], v[238:239], v[148:149]
	v_pk_fma_f32 v[150:151], v[42:43], v[240:241], v[150:151]
	v_pk_fma_f32 v[152:153], v[44:45], v[238:239], v[152:153]
	v_pk_fma_f32 v[154:155], v[34:35], v[240:241], v[154:155]
	v_pk_fma_f32 v[164:165], v[36:37], v[238:239], v[164:165]
	ds_read_b128 v[238:241], v2 offset:14336
	s_waitcnt lgkmcnt(3)
	v_pk_fma_f32 v[8:9], v[76:77], v[244:245], v[8:9]
	v_pk_fma_f32 v[144:145], v[80:81], v[242:243], v[144:145]
	v_pk_fma_f32 v[146:147], v[68:69], v[244:245], v[146:147]
	v_pk_fma_f32 v[148:149], v[72:73], v[242:243], v[148:149]
	v_pk_fma_f32 v[150:151], v[58:59], v[244:245], v[150:151]
	v_pk_fma_f32 v[152:153], v[60:61], v[242:243], v[152:153]
	v_pk_fma_f32 v[154:155], v[46:47], v[244:245], v[154:155]
	v_pk_fma_f32 v[164:165], v[50:51], v[242:243], v[164:165]
	ds_read_b128 v[4:7], v2 offset:15360
	s_waitcnt lgkmcnt(3)
	v_pk_fma_f32 v[8:9], v[96:97], v[232:233], v[8:9]
	v_pk_fma_f32 v[144:145], v[100:101], v[230:231], v[144:145]
	v_pk_fma_f32 v[146:147], v[86:87], v[232:233], v[146:147]
	v_pk_fma_f32 v[148:149], v[88:89], v[230:231], v[148:149]
	v_pk_fma_f32 v[150:151], v[74:75], v[232:233], v[150:151]
	v_pk_fma_f32 v[152:153], v[78:79], v[230:231], v[152:153]
	v_pk_fma_f32 v[154:155], v[66:67], v[232:233], v[154:155]
	v_pk_fma_f32 v[164:165], v[70:71], v[230:231], v[164:165]
	ds_read_b128 v[230:233], v2 offset:16384
	s_waitcnt lgkmcnt(3)
	v_pk_fma_f32 v[8:9], v[112:113], v[236:237], v[8:9]
	v_pk_fma_f32 v[144:145], v[116:117], v[234:235], v[144:145]
	v_pk_fma_f32 v[146:147], v[102:103], v[236:237], v[146:147]
	v_pk_fma_f32 v[148:149], v[104:105], v[234:235], v[148:149]
	v_pk_fma_f32 v[150:151], v[90:91], v[236:237], v[150:151]
	v_pk_fma_f32 v[152:153], v[92:93], v[234:235], v[152:153]
	v_pk_fma_f32 v[154:155], v[82:83], v[236:237], v[154:155]
	v_pk_fma_f32 v[164:165], v[84:85], v[234:235], v[164:165]
	ds_read_b128 v[234:237], v2 offset:17408
	s_waitcnt lgkmcnt(3)
	v_pk_fma_f32 v[8:9], v[126:127], v[240:241], v[8:9]
	v_pk_fma_f32 v[144:145], v[128:129], v[238:239], v[144:145]
	v_pk_fma_f32 v[146:147], v[118:119], v[240:241], v[146:147]
	v_pk_fma_f32 v[148:149], v[120:121], v[238:239], v[148:149]
	v_pk_fma_f32 v[150:151], v[106:107], v[240:241], v[150:151]
	v_pk_fma_f32 v[152:153], v[108:109], v[238:239], v[152:153]
	v_pk_fma_f32 v[154:155], v[94:95], v[240:241], v[154:155]
	v_pk_fma_f32 v[164:165], v[98:99], v[238:239], v[164:165]
	ds_read_b128 v[238:241], v2 offset:18432
	s_waitcnt lgkmcnt(3)
	v_pk_fma_f32 v[8:9], v[140:141], v[6:7], v[8:9]
	v_pk_fma_f32 v[144:145], v[142:143], v[4:5], v[144:145]
	v_pk_fma_f32 v[146:147], v[136:137], v[6:7], v[146:147]
	v_pk_fma_f32 v[150:151], v[122:123], v[6:7], v[150:151]
	v_pk_fma_f32 v[6:7], v[110:111], v[6:7], v[154:155]
	v_pk_mov_b32 v[154:155], v[144:145], v[8:9] op_sel:[1,0]
	v_mov_b32_e32 v145, v9
	v_pk_fma_f32 v[148:149], v[138:139], v[4:5], v[148:149]
	v_pk_add_f32 v[8:9], v[154:155], v[144:145]
	v_pk_fma_f32 v[152:153], v[124:125], v[4:5], v[152:153]
	v_pk_fma_f32 v[4:5], v[114:115], v[4:5], v[164:165]
	v_add_f32_e32 v165, v8, v9
	v_pk_mov_b32 v[8:9], v[148:149], v[146:147] op_sel:[1,0]
	v_mov_b32_e32 v149, v147
	v_pk_add_f32 v[8:9], v[8:9], v[148:149]
	s_nop 0
	v_add_f32_e32 v166, v8, v9
	v_pk_mov_b32 v[8:9], v[152:153], v[150:151] op_sel:[1,0]
	v_mov_b32_e32 v153, v151
	v_pk_add_f32 v[8:9], v[8:9], v[152:153]
	s_nop 0
	v_add_f32_e32 v163, v8, v9
	v_pk_mov_b32 v[8:9], v[4:5], v[6:7] op_sel:[1,0]
	v_mov_b32_e32 v5, v7
	v_pk_add_f32 v[4:5], v[8:9], v[4:5]
	s_nop 0
	v_add_f32_e32 v164, v4, v5
	ds_read_b128 v[242:245], v2 offset:19456
	s_waitcnt lgkmcnt(3)
	v_pk_fma_f32 v[8:9], v[26:27], v[232:233], 0 op_sel_hi:[1,1,0]
	v_pk_fma_f32 v[144:145], v[30:31], v[230:231], 0 op_sel_hi:[1,1,0]
	v_pk_fma_f32 v[146:147], v[20:21], v[232:233], 0 op_sel_hi:[1,1,0]
	v_pk_fma_f32 v[148:149], v[24:25], v[230:231], 0 op_sel_hi:[1,1,0]
	v_pk_fma_f32 v[150:151], v[14:15], v[232:233], 0 op_sel_hi:[1,1,0]
	v_pk_fma_f32 v[152:153], v[16:17], v[230:231], 0 op_sel_hi:[1,1,0]
	v_pk_fma_f32 v[154:155], v[10:11], v[232:233], 0 op_sel_hi:[1,1,0]
	v_pk_fma_f32 v[174:175], v[12:13], v[230:231], 0 op_sel_hi:[1,1,0]
	ds_read_b128 v[230:233], v2 offset:20480
	s_waitcnt lgkmcnt(3)
	v_pk_fma_f32 v[8:9], v[48:49], v[236:237], v[8:9]
	v_pk_fma_f32 v[144:145], v[52:53], v[234:235], v[144:145]
	v_pk_fma_f32 v[146:147], v[38:39], v[236:237], v[146:147]
	v_pk_fma_f32 v[148:149], v[40:41], v[234:235], v[148:149]
	v_pk_fma_f32 v[150:151], v[28:29], v[236:237], v[150:151]
	v_pk_fma_f32 v[152:153], v[32:33], v[234:235], v[152:153]
	v_pk_fma_f32 v[154:155], v[18:19], v[236:237], v[154:155]
	v_pk_fma_f32 v[174:175], v[22:23], v[234:235], v[174:175]
	ds_read_b128 v[234:237], v2 offset:21504
	s_waitcnt lgkmcnt(3)
; __device__ __forceinline__ void ph9_router(const Frame& F, const Args& A) {
;     ...
;             for (int g = 0; g < 4; ++g) { float q[4][4];
; #pragma unroll
;                 for (int el = 0; el < 4; ++el) { f32x4 a0 = {0.f, 0.f, 0.f, 0.f}, a1 = a0, a2 = a0, a3 = a0;
; #pragma unroll
;                     for (int j = 0; j < 8; ++j) { const f32x4 w = wl[(4 * g + el) * 512 + lane + 64 * j];
;                         a0 += hv[0][j] * w; a1 += hv[1][j] * w; a2 += hv[2][j] * w; a3 += hv[3][j] * w; }
;                     q[0][el] = (a0.x + a0.y) + (a0.z + a0.w); q[1][el] = (a1.x + a1.y) + (a1.z + a1.w); q[2][el] = (a2.x + a2.y) + (a2.z + a2.w); q[3][el] = (a3.x + a3.y) + (a3.z + a3.w); }
;                 float s1[2][4], s2[4], s3[2];
; #pragma unroll
;                 for (int k = 0; k < 2; ++k)
; #pragma unroll
;                     for (int el = 0; el < 4; ++el) { const float keep = b4 ? q[2 * k + 1][el] : q[2 * k][el], send = b4 ? q[2 * k][el] : q[2 * k + 1][el]; s1[k][el] = keep + __shfl_xor(send, 16); }
; #pragma unroll
;                 for (int el = 0; el < 4; ++el) { const float keep = b5 ? s1[1][el] : s1[0][el], send = b5 ? s1[0][el] : s1[1][el]; s2[el] = keep + __shfl_xor(send, 32); }
; #pragma unroll
;                 for (int k = 0; k < 2; ++k) { const float keep = b0 ? s2[2 * k + 1] : s2[2 * k], send = b0 ? s2[2 * k] : s2[2 * k + 1]; s3[k] = keep + __shfl_xor(send, 1); }
;                 float s4; { const float keep = b1 ? s3[1] : s3[0], send = b1 ? s3[0] : s3[1]; s4 = keep + __shfl_xor(send, 2); }
;                 s4 += __shfl_xor(s4, 4); s4 += __shfl_xor(s4, 8);
;                 if (((lane >> 2) & 3) == g) mine = s4; }
	v_pk_fma_f32 v[8:9], v[62:63], v[240:241], v[8:9]
	v_pk_fma_f32 v[144:145], v[64:65], v[238:239], v[144:145]
	v_pk_fma_f32 v[146:147], v[54:55], v[240:241], v[146:147]
	v_pk_fma_f32 v[148:149], v[56:57], v[238:239], v[148:149]
	v_pk_fma_f32 v[150:151], v[42:43], v[240:241], v[150:151]
	v_pk_fma_f32 v[152:153], v[44:45], v[238:239], v[152:153]
	v_pk_fma_f32 v[154:155], v[34:35], v[240:241], v[154:155]
	v_pk_fma_f32 v[174:175], v[36:37], v[238:239], v[174:175]
	ds_read_b128 v[238:241], v2 offset:22528
	s_waitcnt lgkmcnt(3)
	v_pk_fma_f32 v[8:9], v[76:77], v[244:245], v[8:9]
	v_pk_fma_f32 v[144:145], v[80:81], v[242:243], v[144:145]
	v_pk_fma_f32 v[146:147], v[68:69], v[244:245], v[146:147]
	v_pk_fma_f32 v[148:149], v[72:73], v[242:243], v[148:149]
	v_pk_fma_f32 v[150:151], v[58:59], v[244:245], v[150:151]
	v_pk_fma_f32 v[152:153], v[60:61], v[242:243], v[152:153]
	v_pk_fma_f32 v[154:155], v[46:47], v[244:245], v[154:155]
	v_pk_fma_f32 v[174:175], v[50:51], v[242:243], v[174:175]
	ds_read_b128 v[4:7], v2 offset:23552
	s_waitcnt lgkmcnt(3)
	v_pk_fma_f32 v[8:9], v[96:97], v[232:233], v[8:9]
	v_pk_fma_f32 v[144:145], v[100:101], v[230:231], v[144:145]
	v_pk_fma_f32 v[146:147], v[86:87], v[232:233], v[146:147]
	v_pk_fma_f32 v[148:149], v[88:89], v[230:231], v[148:149]
	v_pk_fma_f32 v[150:151], v[74:75], v[232:233], v[150:151]
	v_pk_fma_f32 v[152:153], v[78:79], v[230:231], v[152:153]
	v_pk_fma_f32 v[154:155], v[66:67], v[232:233], v[154:155]
	v_pk_fma_f32 v[174:175], v[70:71], v[230:231], v[174:175]
	ds_read_b128 v[230:233], v2 offset:24576
	s_waitcnt lgkmcnt(3)
	v_pk_fma_f32 v[8:9], v[112:113], v[236:237], v[8:9]
	v_pk_fma_f32 v[144:145], v[116:117], v[234:235], v[144:145]
	v_pk_fma_f32 v[146:147], v[102:103], v[236:237], v[146:147]
	v_pk_fma_f32 v[148:149], v[104:105], v[234:235], v[148:149]
	v_pk_fma_f32 v[150:151], v[90:91], v[236:237], v[150:151]
	v_pk_fma_f32 v[152:153], v[92:93], v[234:235], v[152:153]
	v_pk_fma_f32 v[154:155], v[82:83], v[236:237], v[154:155]
	v_pk_fma_f32 v[174:175], v[84:85], v[234:235], v[174:175]
	ds_read_b128 v[234:237], v2 offset:25600
	s_waitcnt lgkmcnt(3)
	v_pk_fma_f32 v[8:9], v[126:127], v[240:241], v[8:9]
	v_pk_fma_f32 v[144:145], v[128:129], v[238:239], v[144:145]
	v_pk_fma_f32 v[146:147], v[118:119], v[240:241], v[146:147]
	v_pk_fma_f32 v[148:149], v[120:121], v[238:239], v[148:149]
	v_pk_fma_f32 v[150:151], v[106:107], v[240:241], v[150:151]
	v_pk_fma_f32 v[152:153], v[108:109], v[238:239], v[152:153]
	v_pk_fma_f32 v[154:155], v[94:95], v[240:241], v[154:155]
	v_pk_fma_f32 v[174:175], v[98:99], v[238:239], v[174:175]
	ds_read_b128 v[238:241], v2 offset:26624
	s_waitcnt lgkmcnt(3)
	v_pk_fma_f32 v[8:9], v[140:141], v[6:7], v[8:9]
	v_pk_fma_f32 v[144:145], v[142:143], v[4:5], v[144:145]
	v_pk_fma_f32 v[146:147], v[136:137], v[6:7], v[146:147]
	v_pk_fma_f32 v[150:151], v[122:123], v[6:7], v[150:151]
	v_pk_fma_f32 v[6:7], v[110:111], v[6:7], v[154:155]
	v_pk_mov_b32 v[154:155], v[144:145], v[8:9] op_sel:[1,0]
	v_mov_b32_e32 v145, v9
	v_pk_fma_f32 v[148:149], v[138:139], v[4:5], v[148:149]
	v_pk_add_f32 v[8:9], v[154:155], v[144:145]
	v_pk_fma_f32 v[152:153], v[124:125], v[4:5], v[152:153]
	v_add_f32_e32 v170, v8, v9
	v_pk_mov_b32 v[8:9], v[148:149], v[146:147] op_sel:[1,0]
	v_mov_b32_e32 v149, v147
	v_pk_add_f32 v[8:9], v[8:9], v[148:149]
	v_pk_fma_f32 v[4:5], v[114:115], v[4:5], v[174:175]
	v_add_f32_e32 v172, v8, v9
	v_pk_mov_b32 v[8:9], v[152:153], v[150:151] op_sel:[1,0]
	v_mov_b32_e32 v153, v151
	v_pk_add_f32 v[8:9], v[8:9], v[152:153]
	s_nop 0
	v_add_f32_e32 v167, v8, v9
	v_pk_mov_b32 v[8:9], v[4:5], v[6:7] op_sel:[1,0]
	v_mov_b32_e32 v5, v7
	v_pk_add_f32 v[4:5], v[8:9], v[4:5]
	s_nop 0
	v_add_f32_e32 v168, v4, v5
	ds_read_b128 v[242:245], v2 offset:27648
	s_waitcnt lgkmcnt(3)
	v_pk_fma_f32 v[8:9], v[26:27], v[232:233], 0 op_sel_hi:[1,1,0]
	v_pk_fma_f32 v[144:145], v[30:31], v[230:231], 0 op_sel_hi:[1,1,0]
	v_pk_fma_f32 v[146:147], v[20:21], v[232:233], 0 op_sel_hi:[1,1,0]
	v_pk_fma_f32 v[148:149], v[24:25], v[230:231], 0 op_sel_hi:[1,1,0]
	v_pk_fma_f32 v[150:151], v[14:15], v[232:233], 0 op_sel_hi:[1,1,0]
	v_pk_fma_f32 v[152:153], v[16:17], v[230:231], 0 op_sel_hi:[1,1,0]
	v_pk_fma_f32 v[154:155], v[10:11], v[232:233], 0 op_sel_hi:[1,1,0]
	v_pk_fma_f32 v[174:175], v[12:13], v[230:231], 0 op_sel_hi:[1,1,0]
	ds_read_b128 v[230:233], v2 offset:28672
	s_waitcnt lgkmcnt(3)
	v_pk_fma_f32 v[8:9], v[48:49], v[236:237], v[8:9]
	v_pk_fma_f32 v[144:145], v[52:53], v[234:235], v[144:145]
	v_pk_fma_f32 v[146:147], v[38:39], v[236:237], v[146:147]
	v_pk_fma_f32 v[148:149], v[40:41], v[234:235], v[148:149]
	v_pk_fma_f32 v[150:151], v[28:29], v[236:237], v[150:151]
	v_pk_fma_f32 v[152:153], v[32:33], v[234:235], v[152:153]
	v_pk_fma_f32 v[154:155], v[18:19], v[236:237], v[154:155]
	v_pk_fma_f32 v[174:175], v[22:23], v[234:235], v[174:175]
	s_waitcnt lgkmcnt(2)
	v_pk_fma_f32 v[8:9], v[62:63], v[240:241], v[8:9]
	v_pk_fma_f32 v[144:145], v[64:65], v[238:239], v[144:145]
	v_pk_fma_f32 v[146:147], v[54:55], v[240:241], v[146:147]
	v_pk_fma_f32 v[148:149], v[56:57], v[238:239], v[148:149]
	v_pk_fma_f32 v[150:151], v[42:43], v[240:241], v[150:151]
	v_pk_fma_f32 v[152:153], v[44:45], v[238:239], v[152:153]
	v_pk_fma_f32 v[154:155], v[34:35], v[240:241], v[154:155]
	v_pk_fma_f32 v[174:175], v[36:37], v[238:239], v[174:175]
	s_waitcnt lgkmcnt(1)
; __device__ __forceinline__ void ph9_router(const Frame& F, const Args& A) {
;     ...
;             for (int g = 0; g < 4; ++g) { float q[4][4];
; #pragma unroll
;                 for (int el = 0; el < 4; ++el) { f32x4 a0 = {0.f, 0.f, 0.f, 0.f}, a1 = a0, a2 = a0, a3 = a0;
; #pragma unroll
;                     for (int j = 0; j < 8; ++j) { const f32x4 w = wl[(4 * g + el) * 512 + lane + 64 * j];
;                         a0 += hv[0][j] * w; a1 += hv[1][j] * w; a2 += hv[2][j] * w; a3 += hv[3][j] * w; }
;                     q[0][el] = (a0.x + a0.y) + (a0.z + a0.w); q[1][el] = (a1.x + a1.y) + (a1.z + a1.w); q[2][el] = (a2.x + a2.y) + (a2.z + a2.w); q[3][el] = (a3.x + a3.y) + (a3.z + a3.w); }
;                 float s1[2][4], s2[4], s3[2];
; #pragma unroll
;                 for (int k = 0; k < 2; ++k)
; #pragma unroll
;                     for (int el = 0; el < 4; ++el) { const float keep = b4 ? q[2 * k + 1][el] : q[2 * k][el], send = b4 ? q[2 * k][el] : q[2 * k + 1][el]; s1[k][el] = keep + __shfl_xor(send, 16); }
; #pragma unroll
;                 for (int el = 0; el < 4; ++el) { const float keep = b5 ? s1[1][el] : s1[0][el], send = b5 ? s1[0][el] : s1[1][el]; s2[el] = keep + __shfl_xor(send, 32); }
; #pragma unroll
;                 for (int k = 0; k < 2; ++k) { const float keep = b0 ? s2[2 * k + 1] : s2[2 * k], send = b0 ? s2[2 * k] : s2[2 * k + 1]; s3[k] = keep + __shfl_xor(send, 1); }
;                 float s4; { const float keep = b1 ? s3[1] : s3[0], send = b1 ? s3[0] : s3[1]; s4 = keep + __shfl_xor(send, 2); }
;                 s4 += __shfl_xor(s4, 4); s4 += __shfl_xor(s4, 8);
;                 if (((lane >> 2) & 3) == g) mine = s4; }
;             const float tot = mine + br[half * 16 + (lane & 15)];
;             if (half == 0) lgv[0] = tot; else lgv[1] = tot;
	v_pk_fma_f32 v[8:9], v[76:77], v[244:245], v[8:9]
	v_pk_fma_f32 v[144:145], v[80:81], v[242:243], v[144:145]
	v_pk_fma_f32 v[146:147], v[68:69], v[244:245], v[146:147]
	v_pk_fma_f32 v[148:149], v[72:73], v[242:243], v[148:149]
	v_pk_fma_f32 v[150:151], v[58:59], v[244:245], v[150:151]
	v_pk_fma_f32 v[152:153], v[60:61], v[242:243], v[152:153]
	v_pk_fma_f32 v[154:155], v[46:47], v[244:245], v[154:155]
	v_pk_fma_f32 v[174:175], v[50:51], v[242:243], v[174:175]
	s_waitcnt lgkmcnt(0)
	v_pk_fma_f32 v[8:9], v[96:97], v[232:233], v[8:9]
	v_pk_fma_f32 v[144:145], v[100:101], v[230:231], v[144:145]
	v_pk_fma_f32 v[146:147], v[86:87], v[232:233], v[146:147]
	v_pk_fma_f32 v[148:149], v[88:89], v[230:231], v[148:149]
	v_pk_fma_f32 v[150:151], v[74:75], v[232:233], v[150:151]
	v_pk_fma_f32 v[152:153], v[78:79], v[230:231], v[152:153]
	v_pk_fma_f32 v[154:155], v[66:67], v[232:233], v[154:155]
	v_pk_fma_f32 v[174:175], v[70:71], v[230:231], v[174:175]
	ds_read_b128 v[4:7], v2 offset:29696
	s_waitcnt lgkmcnt(0)
	v_pk_fma_f32 v[144:145], v[116:117], v[4:5], v[144:145]
	v_pk_fma_f32 v[148:149], v[104:105], v[4:5], v[148:149]
	v_pk_fma_f32 v[152:153], v[92:93], v[4:5], v[152:153]
	v_pk_fma_f32 v[4:5], v[84:85], v[4:5], v[174:175]
	ds_read_b128 v[174:177], v2 offset:30720
	v_pk_fma_f32 v[8:9], v[112:113], v[6:7], v[8:9]
	v_pk_fma_f32 v[146:147], v[102:103], v[6:7], v[146:147]
	v_pk_fma_f32 v[150:151], v[90:91], v[6:7], v[150:151]
	v_pk_fma_f32 v[154:155], v[82:83], v[6:7], v[154:155]
	s_waitcnt lgkmcnt(0)
	v_pk_fma_f32 v[6:7], v[126:127], v[176:177], v[8:9]
	v_pk_fma_f32 v[8:9], v[128:129], v[174:175], v[144:145]
	v_pk_fma_f32 v[144:145], v[118:119], v[176:177], v[146:147]
	v_pk_fma_f32 v[146:147], v[120:121], v[174:175], v[148:149]
	v_pk_fma_f32 v[148:149], v[106:107], v[176:177], v[150:151]
	v_pk_fma_f32 v[150:151], v[108:109], v[174:175], v[152:153]
	v_pk_fma_f32 v[152:153], v[94:95], v[176:177], v[154:155]
	v_pk_fma_f32 v[154:155], v[98:99], v[174:175], v[4:5]
	ds_read_b128 v[2:5], v2 offset:31744
	s_waitcnt lgkmcnt(0)
	v_pk_fma_f32 v[6:7], v[140:141], v[4:5], v[6:7]
	v_pk_fma_f32 v[8:9], v[142:143], v[2:3], v[8:9]
	v_pk_fma_f32 v[144:145], v[136:137], v[4:5], v[144:145]
	v_pk_fma_f32 v[148:149], v[122:123], v[4:5], v[148:149]
	v_pk_fma_f32 v[4:5], v[110:111], v[4:5], v[152:153]
	v_pk_mov_b32 v[152:153], v[8:9], v[6:7] op_sel:[1,0]
	v_mov_b32_e32 v9, v7
	v_pk_fma_f32 v[146:147], v[138:139], v[2:3], v[146:147]
	v_pk_add_f32 v[6:7], v[152:153], v[8:9]
	v_pk_fma_f32 v[150:151], v[124:125], v[2:3], v[150:151]
	v_add_f32_e32 v8, v6, v7
	v_pk_mov_b32 v[6:7], v[146:147], v[144:145] op_sel:[1,0]
	v_mov_b32_e32 v147, v145
	v_pk_add_f32 v[6:7], v[6:7], v[146:147]
	v_pk_fma_f32 v[2:3], v[114:115], v[2:3], v[154:155]
	v_add_f32_e32 v9, v6, v7
	v_pk_mov_b32 v[6:7], v[150:151], v[148:149] op_sel:[1,0]
	v_mov_b32_e32 v151, v149
	v_pk_add_f32 v[6:7], v[6:7], v[150:151]
	s_nop 0
	v_add_f32_e32 v144, v6, v7
	v_pk_mov_b32 v[6:7], v[2:3], v[4:5] op_sel:[1,0]
	v_mov_b32_e32 v3, v5
	v_pk_add_f32 v[2:3], v[6:7], v[2:3]
	v_add_f32_e32 v2, v2, v3
	s_nop 1
	v_permlane16_swap_b32_e32 v161, v162
	v_permlane16_swap_b32_e32 v165, v166
	v_permlane16_swap_b32_e32 v170, v172
	v_permlane16_swap_b32_e32 v8, v9
	v_permlane16_swap_b32_e32 v130, v160
	v_permlane16_swap_b32_e32 v163, v164
	v_permlane16_swap_b32_e32 v167, v168
	v_permlane16_swap_b32_e32 v144, v2
	s_nop 1
	v_add_f32_e32 v3, v161, v162
	v_add_f32_e32 v4, v165, v166
	v_add_f32_e32 v5, v170, v172
	v_add_f32_e32 v6, v8, v9
	v_add_f32_e32 v7, v130, v160
	v_add_f32_e32 v8, v163, v164
	v_add_f32_e32 v9, v167, v168
	v_add_f32_e32 v2, v144, v2
	s_nop 1
	v_permlane32_swap_b32_e32 v3, v7
	v_permlane32_swap_b32_e32 v4, v8
	v_permlane32_swap_b32_e32 v5, v9
	v_permlane32_swap_b32_e32 v6, v2
	s_nop 1
	v_add_f32_e32 v3, v3, v7
	v_add_f32_e32 v4, v4, v8
	v_add_f32_e32 v5, v5, v9
	v_add_f32_e32 v2, v6, v2
	v_cndmask_b32_e64 v6, v4, v3, s[4:5]
	v_cndmask_b32_e64 v7, v3, v4, s[4:5]
	v_cndmask_b32_e64 v8, v2, v5, s[4:5]
	v_cndmask_b32_e64 v9, v5, v2, s[4:5]
	s_nop 1
	v_add_f32_dpp v3, v7, v6 quad_perm:[1,0,3,2] row_mask:0xf bank_mask:0xf
	v_add_f32_dpp v2, v9, v8 quad_perm:[1,0,3,2] row_mask:0xf bank_mask:0xf
	v_cndmask_b32_e64 v4, v2, v3, s[6:7]
	v_cndmask_b32_e64 v5, v3, v2, s[6:7]
	s_nop 1
	v_add_f32_dpp v2, v5, v4 quad_perm:[2,3,0,1] row_mask:0xf bank_mask:0xf
	s_nop 1
	v_mov_b32_dpp v3, v2 row_half_mirror row_mask:0xf bank_mask:0xf
	s_nop 1
	v_add_f32_dpp v2, v3, v2 quad_perm:[3,2,1,0] row_mask:0xf bank_mask:0xf
	s_nop 1
	v_add_f32_dpp v2, v2, v2 row_ror:8 row_mask:0xf bank_mask:0xf
	s_nop 1
	v_cndmask_b32_e32 v159, v159, v2, vcc
	s_cbranch_scc0 .LBB0_1199
	v_or_b32_e32 v130, s42, v156
	v_lshl_add_u64 v[2:3], v[130:131], 2, s[74:75]
	global_load_dword v2, v[2:3], off
	s_mov_b32 s42, 16
	s_and_b64 vcc, exec, s[12:13]
	s_waitcnt vmcnt(0)
	v_add_f32_e32 v2, v159, v2
	v_cndmask_b32_e64 v191, v191, v2, s[0:1]
	v_cndmask_b32_e64 v190, v2, v190, s[0:1]
	s_mov_b64 s[0:1], 0
	s_cbranch_vccnz .LBB0_1202
	s_mov_b64 s[12:13], -1
	s_branch .LBB0_1196
